# attention P.V operand layout: P fragments used in the lane-native k order (8 v_permlane32_swap per tile and wave removed in all six tile bodies), V tile staged without the key bit-2/3 exchange to matc
# baseline (speedup 1.0000x reference)
; __device__ __forceinline__ int v_st(int k, int c) { const int kk = (k & ~0xC) | ((k & 4) << 1) | ((k & 8) >> 1); return ((kk >> 3) * 4 + (c >> 5)) * 512 + ((kk & 7) * 32 + (c & 31)) * 2; }
; __device__ __forceinline__ int v_rd_base(int lane) { return ((lane & 3) << 3) | (((lane >> 2) & 3) << 6) | (((lane >> 4) & 1) << 5) | (((lane >> 5) & 1) << 8); }
; template <int DK, bool PF, bool EARLY, bool PFD = false> ...
;     ...
;     const int tid = threadIdx.x, lane = tid & 63, r32 = lane & 31, hi = lane >> 5;
;     char* V_lds = lds_kv; char* K_lds = lds_kv + 2 * SHM_V;
;     bf16x8 qr[NQ];
; #pragma unroll
;     for (int d0 = 0; d0 < NQ; ++d0) qr[d0] = *reinterpret_cast<const bf16x8*>(Qrow + d0 * 16);
;     const __amdgpu_buffer_rsrc_t krs = __builtin_amdgcn_make_buffer_rsrc((void*)Kh, 0, nkeys * ldk * 2, 0x00020000);
;     const __amdgpu_buffer_rsrc_t vrs = __builtin_amdgcn_make_buffer_rsrc((void*)Vh, 0, nkeys * ldv * 2, 0x00020000);
;     unsigned kgo[KP]; int kst[KP];
; #pragma unroll
;     for (int i = 0; i < KP; ++i) { const int p = tid + i * NT, row = p / CH, ch = p % CH; kgo[i] = (unsigned)(row * ldk + ch * 8) * 2u; kst[i] = kswz<DK>(row, ch); }
;     const int vrow0 = tid >> 4, vc = (tid & 15) * 8;
;     const unsigned vgo = (unsigned)(vrow0 * ldv + vc) * 2u, vstep = (unsigned)(32 * ldv) * 2u;
;     const int vst0 = v_st(vrow0, vc); constexpr int vst1d = 8192;
;     const int vb0 = (int)(uintptr_t)V_lds + v_rd_base(lane);
;     const int kbase = r32 * (DK * 2), kt0 = (hi ^ ((r32 >> 1) & 7)) << 4;
; __device__ __forceinline__ void mla_attn_unit(const Ptrs& P, unsigned char* lds, int b, int h, int qb, int ctxq, unsigned& sacc) {
;     ...
;     const int tid = threadIdx.x, wid = tid >> 6, lane = tid & 63, r32 = lane & 31, hi = lane >> 5;
;     const bf16* Qm = (const bf16*)(P.ws + WS_QM); const bf16* Km = (const bf16*)(P.ws + WS_KM); const bf16* Vm = (const bf16*)(P.ws + WS_VM);
;     const size_t u0 = (size_t)b * SU + (ctxq ? 0 : CTX) + qb * 256 + wid * 32;
;     f32x16 o[4] = {}; float l_reg = 0.f;
;     const float negM = -((const float*)(P.ws + WS_SCAL))[0];
;     attn_loop<192, false, false>(Qm + (u0 + r32) * 768 + h * 192 + hi * 8, Km + (size_t)b * SU * 768 + h * 192, 768, Vm + (size_t)b * SU * 512 + h * 128, 512, ctxq ? CTX : SU, negM, o, l_reg, (char*)lds, sacc);
.LBB0_1184:
	v_readlane_b32 s0, v254, 2
	s_cmpk_gt_i32 s0, 0x10f
	s_waitcnt vmcnt(0)
	s_barrier
	s_cbranch_scc1 .LBB0_1203
	v_mul_u32_u24_e32 v4, 0xaab, v0
	v_mov_b32_e32 v5, 24
	v_mul_lo_u16_sdwa v6, v4, v5 dst_sel:DWORD dst_unused:UNUSED_PAD src0_sel:WORD_1 src1_sel:DWORD
	s_movk_i32 s45, 0x600
	v_sub_u16_e32 v6, v0, v6
	v_mul_u32_u24_sdwa v7, v4, s45 dst_sel:DWORD dst_unused:UNUSED_PAD src0_sel:WORD_1 src1_sel:DWORD
	s_movk_i32 s6, 0x180
	v_lshl_or_b32 v185, v6, 4, v7
	v_mul_u32_u24_sdwa v7, v4, s6 dst_sel:DWORD dst_unused:UNUSED_PAD src0_sel:WORD_1 src1_sel:DWORD
	v_lshrrev_b32_e32 v4, 17, v4
	v_bitop3_b32 v4, v4, v6, 7 bitop3:0x6c
	s_movk_i32 s4, 0xaab
	v_lshl_add_u32 v187, v4, 4, v7
	v_or_b32_e32 v4, 0x200, v0
	v_mul_u32_u24_sdwa v6, v4, s4 dst_sel:DWORD dst_unused:UNUSED_PAD src0_sel:WORD_0 src1_sel:DWORD
	v_mul_lo_u16_sdwa v7, v6, v5 dst_sel:DWORD dst_unused:UNUSED_PAD src0_sel:WORD_1 src1_sel:DWORD
	v_sub_u16_e32 v4, v4, v7
	v_mul_u32_u24_sdwa v7, v6, s45 dst_sel:DWORD dst_unused:UNUSED_PAD src0_sel:WORD_1 src1_sel:DWORD
	v_lshl_or_b32 v191, v4, 4, v7
	v_mul_u32_u24_sdwa v7, v6, s6 dst_sel:DWORD dst_unused:UNUSED_PAD src0_sel:WORD_1 src1_sel:DWORD
	v_lshrrev_b32_e32 v6, 17, v6
	v_bitop3_b32 v4, v6, v4, 7 bitop3:0x6c
	v_lshl_add_u32 v193, v4, 4, v7
	v_or_b32_e32 v4, 0x400, v0
	v_mul_u32_u24_sdwa v6, v4, s4 dst_sel:DWORD dst_unused:UNUSED_PAD src0_sel:WORD_0 src1_sel:DWORD
	v_mul_lo_u16_sdwa v5, v6, v5 dst_sel:DWORD dst_unused:UNUSED_PAD src0_sel:WORD_1 src1_sel:DWORD
	v_sub_u16_e32 v4, v4, v5
	v_mul_u32_u24_sdwa v5, v6, s45 dst_sel:DWORD dst_unused:UNUSED_PAD src0_sel:WORD_1 src1_sel:DWORD
	v_lshl_or_b32 v195, v4, 4, v5
	v_mul_u32_u24_sdwa v5, v6, s6 dst_sel:DWORD dst_unused:UNUSED_PAD src0_sel:WORD_1 src1_sel:DWORD
	v_lshrrev_b32_e32 v6, 17, v6
	v_bitop3_b32 v4, v6, v4, 7 bitop3:0x6c
	s_add_u32 s0, s78, 0x257ce000
	v_lshl_add_u32 v197, v4, 4, v5
	v_lshlrev_b32_e32 v5, 3, v0
	s_addc_u32 s1, s79, 0
	v_and_b32_e32 v192, 0x78, v5
	s_add_u32 s3, s78, 0x2714e000
	v_lshrrev_b32_e32 v4, 4, v0
	v_lshlrev_b32_e32 v6, 1, v192
	s_addc_u32 s42, s79, 0
	v_lshl_or_b32 v199, v4, 10, v6
	v_and_b32_e32 v4, 16, v4
	v_lshrrev_b32_e32 v7, 3, v0
	s_add_u32 s43, s78, 0x28ace000
	v_and_or_b32 v4, v7, 8, v4
	s_addc_u32 s44, s79, 0
	v_lshrrev_b32_e32 v3, 5, v0
	v_lshrrev_b32_e32 v4, 1, v4
	v_bfe_u32 v7, v5, 5, 2
	v_bfe_u32 v11, v0, 1, 3
	s_add_u32 s36, s78, 0x13c000
	v_or_b32_e32 v4, v4, v7
	v_and_or_b32 v7, v3, 4, v71
	v_bitop3_b32 v3, v3, v11, 1 bitop3:0x6c
	s_addc_u32 s37, s79, 0
	v_lshlrev_b32_e32 v7, 6, v7
	v_and_b32_e32 v8, 48, v6
	v_lshlrev_b32_e32 v201, 4, v3
	v_lshl_add_u32 v3, v4, 9, 0
	v_lshlrev_b32_e32 v9, 4, v0
	v_lshlrev_b32_e32 v10, 1, v0
	v_add3_u32 v205, v3, v7, v8
	v_lshrrev_b32_e32 v253, 3, v205
	v_xor_b32_e32 v253, v253, v205
	v_and_b32_e32 v253, 0x100, v253
	v_xor_b32_e32 v205, v205, v253
	v_lshlrev_b32_e32 v253, 3, v253
	v_xor_b32_e32 v205, v205, v253
	v_and_b32_e32 v3, 0x118, v5
	s_cmp_lg_u32 0, -1
	v_and_b32_e32 v9, 0xc0, v9
	v_mad_u32_u24 v207, v184, s6, 0
	v_and_or_b32 v3, v10, 32, v3
	s_cselect_b32 s6, 0, 0
	v_lshrrev_b32_e32 v2, 5, v182
	v_add3_u32 v209, v9, s6, v3
	v_and_b32_e32 v3, 0x1c0, v0
	s_add_i32 s6, 0, 0x1f800
	v_lshlrev_b32_e32 v190, 3, v2
	v_lshl_add_u32 v226, v3, 2, s6
	v_lshlrev_b32_e32 v228, 4, v2
	v_lshl_add_u32 v3, v1, 13, 0
	v_lshlrev_b32_e32 v4, 1, v184
	v_lshlrev_b32_e32 v2, 10, v2
	v_add3_u32 v229, v3, v4, v2
	v_or_b32_e32 v2, 4, v71
	v_lshlrev_b32_e32 v232, 8, v2
	v_lshlrev_b32_e32 v196, 10, v2
	v_or_b32_e32 v2, 8, v71
	v_lshlrev_b32_e32 v233, 8, v2
	v_lshlrev_b32_e32 v198, 10, v2
	v_or_b32_e32 v2, 12, v71
	v_lshlrev_b32_e32 v234, 8, v2
	v_lshlrev_b32_e32 v200, 10, v2
	v_or_b32_e32 v2, 16, v71
	v_lshlrev_b32_e32 v235, 8, v2
	v_lshlrev_b32_e32 v202, 10, v2
	v_or_b32_e32 v2, 20, v71
	v_xor_b32_e32 v214, 32, v201
	v_xor_b32_e32 v215, 64, v201
	v_xor_b32_e32 v216, 0x60, v201
	v_lshlrev_b32_e32 v236, 8, v2
	v_lshlrev_b32_e32 v204, 10, v2
	v_or_b32_e32 v2, 24, v71
	v_lshlrev_b32_e32 v186, 5, v1
	v_mov_b32_e32 v189, 0
	s_movk_i32 s4, 0xff
	v_add_u32_e32 v217, v207, v201
	v_add_u32_e32 v219, v207, v214
	v_add_u32_e32 v221, v207, v215
	v_add_u32_e32 v223, v207, v216
	v_lshlrev_b32_e32 v237, 8, v2
	v_lshlrev_b32_e32 v206, 10, v2
	v_or_b32_e32 v2, 28, v71
	v_cmp_lt_u32_e64 s[4:5], s4, v0
	v_or_b32_e32 v203, 0x8000, v199
	s_mov_b32 s39, 0
	v_add_u32_e32 v218, 0xe000, v217
	v_add_u32_e32 v220, 0xe000, v219
	v_add_u32_e32 v222, 0xe000, v221
	v_add_u32_e32 v224, 0xe000, v223
	v_add_u32_e32 v225, 0x4000, v209
	v_cmp_gt_u32_e64 s[6:7], 32, v182
	v_lshl_add_u32 v227, v184, 2, v226
	v_add_u32_e32 v230, v3, v6
	v_lshlrev_b32_e32 v231, 8, v71
	v_lshlrev_b32_e32 v194, 10, v71
	v_lshlrev_b32_e32 v238, 8, v2
	v_lshlrev_b32_e32 v208, 10, v2
	v_or_b32_e32 v210, 0x100, v186
	v_mov_b32_e32 v211, v189
	s_mov_b32 s10, 0x660000
	s_mov_b32 s14, 0x440000
	s_mov_b32 s11, 0x20000
	s_mov_b32 s18, 0x60000
	s_mov_b32 s22, 0x40000
	s_movk_i32 s46, 0x7fff
	s_mov_b64 s[40:41], 0x29cde400
	v_mov_b32_e32 v239, 0x600
	v_readlane_b32 s47, v254, 2
	s_branch .LBB0_1188

; #define PSUB_AT(k) do { if (PROBE_SUB == (k) && DK == PROBE_SUBDK) sacc = __builtin_amdgcn_readfirstlane(sacc + ((unsigned)__builtin_readcyclecounter() - ps_t0_)); } while (0)
; #define SBAR() __builtin_amdgcn_sched_barrier(0)
; #define SLOAD(k0) do { const unsigned so_k = (unsigned)((k0) * ldk) * 2u, so_v = (unsigned)((k0) * ldv) * 2u; \
;         _Pragma("unroll") for (int i = 0; i < KP; ++i) ks[i] = __builtin_amdgcn_raw_buffer_load_b128(krs, kgo[i], so_k, 0); \
;         vs0 = __builtin_amdgcn_raw_buffer_load_b128(vrs, vgo, so_v, 0); vs1 = __builtin_amdgcn_raw_buffer_load_b128(vrs, vgo + vstep, so_v, 0); } while (0)
; template <int DK, bool PF, bool EARLY, bool PFD = false> ...
;     ...
;         if (EARLY && j + 1 < ntile) SLOAD((j + 1) * 64);
;         f32x16 p0, p1;
; #pragma unroll
;         for (int r = 0; r < 16; ++r) { p0[r] = negM; p1[r] = negM; }
;         const char* Kb = K_lds + cur * SHM_K;
; #pragma unroll
;         for (int d0 = 0; d0 < NQ; ++d0) {
;             const bf16x8 b0 = *reinterpret_cast<const bf16x8*>(Kb + kra_(d0 & 3) + (d0 >> 2) * 128);
;             const bf16x8 b1 = *reinterpret_cast<const bf16x8*>(Kb + kra_(d0 & 3) + (d0 >> 2) * 128 + 32 * DK * 2);
;             p0 = __builtin_amdgcn_mfma_f32_32x32x16_bf16(b0, qr[d0], p0, 0, 0, 0);
;             p1 = __builtin_amdgcn_mfma_f32_32x32x16_bf16(b1, qr[d0], p1, 0, 0, 0);
;             if ((d0 & 3) == 3) SBAR();
;         }
;         PSUB_AT(1);
;         if (!EARLY && j + 1 < ntile) SLOAD((j + 1) * 64);
;         float ps = 0.f, ps1 = 0.f;
; #pragma unroll
;         for (int r = 0; r < 16; ++r) { p0[r] = __builtin_amdgcn_exp2f(p0[r]); p1[r] = __builtin_amdgcn_exp2f(p1[r]); ps += p0[r]; asm("" : "+v"(ps)); ps1 += p1[r]; asm("" : "+v"(ps1)); }
;         l_reg += ps + ps1;
;         bf16x8 pa0, pa1, pa2, pa3;
;     ...
;         PK4(p0, 0, pa0); PK4(p0, 8, pa1); PK4(p1, 0, pa2); PK4(p1, 8, pa3);
;     ...
;         PSUB_AT(2);
;         const int vb = vb0 + cur * SHM_V;
.LBB0_1192:
	s_and_b32 s15, s8, 1
	s_mul_i32 s16, s15, 0x6000
	v_add_u32_e32 v170, s16, v207
	v_add_u32_e32 v171, v170, v201
	ds_read_b128 v[82:85], v171 offset:32768
	ds_read_b128 v[162:165], v171 offset:45056
	v_add_u32_e32 v172, v170, v214
	v_add_u32_e32 v173, v170, v215
	v_add_u32_e32 v170, v170, v216
	s_waitcnt lgkmcnt(1)
	v_mfma_f32_32x32x16_bf16 v[98:113], v[82:85], v[158:161], v[66:81]
	s_waitcnt lgkmcnt(0)
	v_mfma_f32_32x32x16_bf16 v[82:97], v[162:165], v[158:161], v[66:81]
	ds_read_b128 v[162:165], v172 offset:32768
	ds_read_b128 v[166:169], v172 offset:45056
	s_waitcnt lgkmcnt(1)
	v_mfma_f32_32x32x16_bf16 v[98:113], v[162:165], v[154:157], v[98:113]
	s_waitcnt lgkmcnt(0)
	v_mfma_f32_32x32x16_bf16 v[82:97], v[166:169], v[154:157], v[82:97]
	ds_read_b128 v[162:165], v173 offset:32768
	ds_read_b128 v[166:169], v173 offset:45056
	s_waitcnt lgkmcnt(1)
	v_mfma_f32_32x32x16_bf16 v[98:113], v[162:165], v[150:153], v[98:113]
	s_waitcnt lgkmcnt(0)
	v_mfma_f32_32x32x16_bf16 v[82:97], v[166:169], v[150:153], v[82:97]
	ds_read_b128 v[162:165], v170 offset:32768
	ds_read_b128 v[166:169], v170 offset:45056
	s_waitcnt lgkmcnt(1)
	v_mfma_f32_32x32x16_bf16 v[98:113], v[162:165], v[146:149], v[98:113]
	s_waitcnt lgkmcnt(0)
	v_mfma_f32_32x32x16_bf16 v[82:97], v[166:169], v[146:149], v[82:97]
	ds_read_b128 v[162:165], v171 offset:32896
	ds_read_b128 v[166:169], v171 offset:45184
	s_waitcnt lgkmcnt(1)
	v_mfma_f32_32x32x16_bf16 v[98:113], v[162:165], v[142:145], v[98:113]
	ds_read_b128 v[162:165], v172 offset:32896
	s_waitcnt lgkmcnt(1)
	v_mfma_f32_32x32x16_bf16 v[82:97], v[166:169], v[142:145], v[82:97]
	s_waitcnt lgkmcnt(0)
	v_mfma_f32_32x32x16_bf16 v[98:113], v[162:165], v[138:141], v[98:113]
	ds_read_b128 v[162:165], v172 offset:45184
	s_waitcnt lgkmcnt(0)
	v_mfma_f32_32x32x16_bf16 v[82:97], v[162:165], v[138:141], v[82:97]
	ds_read_b128 v[162:165], v173 offset:32896
	s_waitcnt lgkmcnt(0)
	v_mfma_f32_32x32x16_bf16 v[98:113], v[162:165], v[134:137], v[98:113]
	ds_read_b128 v[162:165], v173 offset:45184
	s_waitcnt lgkmcnt(0)
	v_mfma_f32_32x32x16_bf16 v[82:97], v[162:165], v[134:137], v[82:97]
	ds_read_b128 v[162:165], v170 offset:32896
	s_waitcnt lgkmcnt(0)
	v_mfma_f32_32x32x16_bf16 v[98:113], v[162:165], v[130:133], v[98:113]
	ds_read_b128 v[162:165], v170 offset:45184
	s_waitcnt lgkmcnt(0)
	v_mfma_f32_32x32x16_bf16 v[82:97], v[162:165], v[130:133], v[82:97]
	ds_read_b128 v[162:165], v171 offset:33024
	ds_read_b128 v[166:169], v171 offset:45312
	s_waitcnt lgkmcnt(1)
	v_mfma_f32_32x32x16_bf16 v[98:113], v[162:165], v[126:129], v[98:113]
	ds_read_b128 v[162:165], v172 offset:33024
	s_waitcnt lgkmcnt(1)
	v_mfma_f32_32x32x16_bf16 v[82:97], v[166:169], v[126:129], v[82:97]
	s_waitcnt lgkmcnt(0)
	v_mfma_f32_32x32x16_bf16 v[98:113], v[162:165], v[122:125], v[98:113]
	ds_read_b128 v[162:165], v172 offset:45312
	s_waitcnt lgkmcnt(0)
	v_mfma_f32_32x32x16_bf16 v[82:97], v[162:165], v[122:125], v[82:97]
	ds_read_b128 v[162:165], v173 offset:33024
	s_waitcnt lgkmcnt(0)
	v_mfma_f32_32x32x16_bf16 v[98:113], v[162:165], v[118:121], v[98:113]
	ds_read_b128 v[162:165], v173 offset:45312
	s_waitcnt lgkmcnt(0)
	v_mfma_f32_32x32x16_bf16 v[82:97], v[162:165], v[118:121], v[82:97]
	ds_read_b128 v[162:165], v170 offset:33024
	s_waitcnt lgkmcnt(0)
	v_mfma_f32_32x32x16_bf16 v[98:113], v[162:165], v[114:117], v[98:113]
	ds_read_b128 v[162:165], v170 offset:45312
	s_waitcnt lgkmcnt(0)
	v_mfma_f32_32x32x16_bf16 v[82:97], v[162:165], v[114:117], v[82:97]
	buffer_load_dwordx4 v[178:181], v185, s[24:27], s9 offen
	buffer_load_dwordx4 v[170:173], v191, s[24:27], s9 offen
	buffer_load_dwordx4 v[174:177], v195, s[24:27], s9 offen
	buffer_load_dwordx4 v[162:165], v199, s[28:31], s13 offen
	buffer_load_dwordx4 v[166:169], v203, s[28:31], s13 offen
	s_nop 6
	v_exp_f32_e32 v241, v82
	v_exp_f32_e32 v98, v98
	v_exp_f32_e32 v243, v83
	v_exp_f32_e32 v99, v99
	v_add_f32_e32 v242, 0, v241
	v_add_f32_e32 v82, 0, v98
	v_exp_f32_e32 v83, v100
	v_add_f32_e32 v100, v243, v242
	v_exp_f32_e32 v242, v84
	v_add_f32_e32 v82, v99, v82
	v_exp_f32_e32 v84, v101
	v_exp_f32_e32 v101, v85
	v_add_f32_e32 v82, v83, v82
	v_exp_f32_e32 v85, v102
	v_add_f32_e32 v100, v242, v100
	v_exp_f32_e32 v102, v86
	v_add_f32_e32 v82, v84, v82
	v_exp_f32_e32 v86, v103
	v_add_f32_e32 v100, v101, v100
	v_exp_f32_e32 v103, v87
	v_add_f32_e32 v82, v85, v82
	v_exp_f32_e32 v87, v104
	v_add_f32_e32 v100, v102, v100
	v_exp_f32_e32 v104, v88
	v_add_f32_e32 v82, v86, v82
	v_exp_f32_e32 v88, v105
	v_add_f32_e32 v100, v103, v100
	v_exp_f32_e32 v105, v89
	v_add_f32_e32 v82, v87, v82
	v_exp_f32_e32 v89, v106
	v_add_f32_e32 v100, v104, v100
	v_exp_f32_e32 v106, v90
	v_add_f32_e32 v82, v88, v82
	v_exp_f32_e32 v90, v107
	v_add_f32_e32 v100, v105, v100
	v_exp_f32_e32 v107, v91
	v_add_f32_e32 v82, v89, v82
	v_exp_f32_e32 v91, v108
	v_add_f32_e32 v100, v106, v100
	v_exp_f32_e32 v108, v92
	v_add_f32_e32 v82, v90, v82
	v_exp_f32_e32 v92, v109
	v_add_f32_e32 v100, v107, v100
	v_exp_f32_e32 v109, v93
	v_add_f32_e32 v82, v91, v82
	v_exp_f32_e32 v93, v110
	v_add_f32_e32 v100, v108, v100
	v_exp_f32_e32 v110, v94
	v_add_f32_e32 v82, v92, v82
	v_exp_f32_e32 v94, v111
	v_add_f32_e32 v100, v109, v100
	v_exp_f32_e32 v111, v95
	v_add_f32_e32 v82, v93, v82
	v_exp_f32_e32 v95, v112
	v_add_f32_e32 v100, v110, v100
	v_exp_f32_e32 v112, v96
	v_add_f32_e32 v82, v94, v82
	v_exp_f32_e32 v96, v113
	v_add_f32_e32 v100, v111, v100
	v_exp_f32_e32 v97, v97
	v_add_f32_e32 v82, v95, v82
	v_add_f32_e32 v100, v112, v100
	v_add_f32_e32 v82, v96, v82
	v_add_f32_e32 v100, v97, v100
	s_lshl_b32 s16, s15, 14
	v_add_f32_e32 v82, v82, v100
	v_add_f32_e32 v240, v240, v82
	v_cvt_pk_bf16_f32 v82, v98, v99
	v_cvt_pk_bf16_f32 v83, v83, v84
	v_cvt_pk_bf16_f32 v84, v85, v86
	v_cvt_pk_bf16_f32 v85, v87, v88
	v_cvt_pk_bf16_f32 v86, v89, v90
	v_cvt_pk_bf16_f32 v87, v91, v92
	v_cvt_pk_bf16_f32 v88, v93, v94
	v_cvt_pk_bf16_f32 v89, v95, v96
	v_cvt_pk_bf16_f32 v90, v241, v243
	v_cvt_pk_bf16_f32 v91, v242, v101
	v_cvt_pk_bf16_f32 v92, v102, v103
	v_cvt_pk_bf16_f32 v93, v104, v105
	v_cvt_pk_bf16_f32 v94, v106, v107
	v_cvt_pk_bf16_f32 v95, v108, v109
	v_cvt_pk_bf16_f32 v96, v110, v111
	v_cvt_pk_bf16_f32 v97, v112, v97
	v_add_u32_e32 v241, s16, v209
	ds_read_b64_tr_b16 v[98:99], v241 offset:0
	ds_read_b64_tr_b16 v[100:101], v241 offset:0x800
	ds_read_b64_tr_b16 v[102:103], v241 offset:0x1000
	ds_read_b64_tr_b16 v[104:105], v241 offset:0x1800
	ds_read_b64_tr_b16 v[106:107], v241 offset:0x2000
	ds_read_b64_tr_b16 v[108:109], v241 offset:0x2800
	ds_read_b64_tr_b16 v[110:111], v241 offset:0x3000
	ds_read_b64_tr_b16 v[112:113], v241 offset:0x3800
	s_waitcnt lgkmcnt(0)
; #define PSUB_AT(k) do { if (PROBE_SUB == (k) && DK == PROBE_SUBDK) sacc = __builtin_amdgcn_readfirstlane(sacc + ((unsigned)__builtin_readcyclecounter() - ps_t0_)); } while (0)
; #define SBAR() __builtin_amdgcn_sched_barrier(0)
; #define SWRITE(b) do { _Pragma("unroll") for (int i = 0; i < KP; ++i) *reinterpret_cast<u32x4*>(K_lds + (b) * SHM_K + kst[i]) = ks[i]; \
;         *reinterpret_cast<u32x4*>(V_lds + (b) * SHM_V + vst0) = vs0; *reinterpret_cast<u32x4*>(V_lds + (b) * SHM_V + vst0 + vst1d) = vs1; } while (0)
; template <int DK, bool PF, bool EARLY, bool PFD = false> ...
;     ...
; #pragma unroll
;         for (int d0 = 0; d0 < NQ; ++d0) {
;             const bf16x8 b0 = *reinterpret_cast<const bf16x8*>(Kb + kra_(d0 & 3) + (d0 >> 2) * 128);
;             const bf16x8 b1 = *reinterpret_cast<const bf16x8*>(Kb + kra_(d0 & 3) + (d0 >> 2) * 128 + 32 * DK * 2);
;             p0 = __builtin_amdgcn_mfma_f32_32x32x16_bf16(b0, qr[d0], p0, 0, 0, 0);
;             p1 = __builtin_amdgcn_mfma_f32_32x32x16_bf16(b1, qr[d0], p1, 0, 0, 0);
;             if ((d0 & 3) == 3) SBAR();
;     ...
;         PK4(p0, 0, pa0); PK4(p0, 8, pa1); PK4(p1, 0, pa2); PK4(p1, 8, pa3);
;     ...
;         PSUB_AT(2);
;         const int vb = vb0 + cur * SHM_V;
;         pv_one<0>(o[0], vb, pa0, pa1, pa2, pa3); pv_one<1>(o[1], vb, pa0, pa1, pa2, pa3); pv_one<2>(o[2], vb, pa0, pa1, pa2, pa3); pv_one<3>(o[3], vb, pa0, pa1, pa2, pa3);
;         PSUB_AT(3);
;         if (j + 1 < ntile) SWRITE(cur ^ 1);
;         if (j + 3 < ntile) PREFETCH(j + 3);
;         __syncthreads();
	s_add_i32 s8, s8, 1
	v_mfma_f32_32x32x16_bf16 v[2:17], v[82:85], v[98:101], v[2:17]
	ds_read_b64_tr_b16 v[98:99], v241 offset:0x200
	ds_read_b64_tr_b16 v[100:101], v241 offset:0xa00
	v_mfma_f32_32x32x16_bf16 v[2:17], v[86:89], v[102:105], v[2:17]
	ds_read_b64_tr_b16 v[102:103], v241 offset:0x1200
	ds_read_b64_tr_b16 v[104:105], v241 offset:0x1a00
	v_mfma_f32_32x32x16_bf16 v[2:17], v[90:93], v[106:109], v[2:17]
	ds_read_b64_tr_b16 v[106:107], v241 offset:0x2200
	ds_read_b64_tr_b16 v[108:109], v241 offset:0x2a00
	ds_read_b64_tr_b16 v[242:243], v241 offset:0x3200
	ds_read_b64_tr_b16 v[244:245], v241 offset:0x3a00
	s_waitcnt lgkmcnt(0)
	v_mfma_f32_32x32x16_bf16 v[2:17], v[94:97], v[110:113], v[2:17]
	v_mfma_f32_32x32x16_bf16 v[18:33], v[82:85], v[98:101], v[18:33]
	ds_read_b64_tr_b16 v[98:99], v241 offset:0x400
	ds_read_b64_tr_b16 v[100:101], v241 offset:0xc00
	v_mfma_f32_32x32x16_bf16 v[18:33], v[86:89], v[102:105], v[18:33]
	ds_read_b64_tr_b16 v[102:103], v241 offset:0x1400
	ds_read_b64_tr_b16 v[104:105], v241 offset:0x1c00
	v_mfma_f32_32x32x16_bf16 v[18:33], v[90:93], v[106:109], v[18:33]
	ds_read_b64_tr_b16 v[106:107], v241 offset:0x2400
	ds_read_b64_tr_b16 v[108:109], v241 offset:0x2c00
	ds_read_b64_tr_b16 v[110:111], v241 offset:0x3400
	ds_read_b64_tr_b16 v[112:113], v241 offset:0x3c00
	s_waitcnt lgkmcnt(0)
	v_mfma_f32_32x32x16_bf16 v[18:33], v[94:97], v[242:245], v[18:33]
	v_mfma_f32_32x32x16_bf16 v[34:49], v[82:85], v[98:101], v[34:49]
	ds_read_b64_tr_b16 v[98:99], v241 offset:0x600
	ds_read_b64_tr_b16 v[100:101], v241 offset:0xe00
	v_mfma_f32_32x32x16_bf16 v[34:49], v[86:89], v[102:105], v[34:49]
	ds_read_b64_tr_b16 v[102:103], v241 offset:0x1600
	ds_read_b64_tr_b16 v[104:105], v241 offset:0x1e00
	v_mfma_f32_32x32x16_bf16 v[34:49], v[90:93], v[106:109], v[34:49]
	ds_read_b64_tr_b16 v[106:107], v241 offset:0x2600
	ds_read_b64_tr_b16 v[108:109], v241 offset:0x2e00
	ds_read_b64_tr_b16 v[242:243], v241 offset:0x3600
	ds_read_b64_tr_b16 v[244:245], v241 offset:0x3e00
	s_waitcnt lgkmcnt(0)
	v_mfma_f32_32x32x16_bf16 v[34:49], v[94:97], v[110:113], v[34:49]
	v_mfma_f32_32x32x16_bf16 v[50:65], v[82:85], v[98:101], v[50:65]
	s_xor_b32 s15, s15, 1
	s_mulk_i32 s15, 0x6000
	s_add_i32 s15, s15, 0
	v_add_u32_e32 v82, s15, v187
	s_waitcnt vmcnt(4)
	ds_write_b128 v82, v[178:181] offset:32768
	v_add_u32_e32 v82, s15, v193
	s_waitcnt vmcnt(3)
	ds_write_b128 v82, v[170:173] offset:32768
	v_mfma_f32_32x32x16_bf16 v[50:65], v[86:89], v[102:105], v[50:65]
	v_add_u32_e32 v82, s15, v197
	s_xor_b32 s15, s16, 0x4000
	s_add_i32 s9, s9, 0x18000
	s_add_i32 s13, s13, 0x10000
	v_add_u32_e32 v83, s15, v205
	s_cmp_eq_u32 s9, 0x60000
	s_waitcnt vmcnt(2)
	ds_write_b128 v82, v[174:177] offset:32768
	v_mfma_f32_32x32x16_bf16 v[50:65], v[90:93], v[106:109], v[50:65]
	s_waitcnt vmcnt(1)
	ds_write_b128 v83, v[162:165]
	s_waitcnt vmcnt(0)
	ds_write_b128 v83, v[166:169] offset:8192
	s_waitcnt lgkmcnt(0)
	s_barrier
	v_mfma_f32_32x32x16_bf16 v[50:65], v[94:97], v[242:245], v[50:65]
	s_cbranch_scc0 .LBB0_1192
	ds_read_b128 v[98:101], v217 offset:57344
	ds_read_b128 v[102:105], v218 offset:12288
	s_waitcnt lgkmcnt(1)
	v_mfma_f32_32x32x16_bf16 v[82:97], v[98:101], v[158:161], v[66:81]
	ds_read_b128 v[98:101], v219 offset:57344
	s_waitcnt lgkmcnt(1)
	v_mfma_f32_32x32x16_bf16 v[66:81], v[102:105], v[158:161], v[66:81]
	s_waitcnt lgkmcnt(0)
	v_mfma_f32_32x32x16_bf16 v[82:97], v[98:101], v[154:157], v[82:97]
	ds_read_b128 v[98:101], v220 offset:12288
	s_waitcnt lgkmcnt(0)
	v_mfma_f32_32x32x16_bf16 v[66:81], v[98:101], v[154:157], v[66:81]
	ds_read_b128 v[98:101], v221 offset:57344
	s_waitcnt lgkmcnt(0)
	v_mfma_f32_32x32x16_bf16 v[82:97], v[98:101], v[150:153], v[82:97]
	ds_read_b128 v[98:101], v222 offset:12288
	s_waitcnt lgkmcnt(0)
	v_mfma_f32_32x32x16_bf16 v[66:81], v[98:101], v[150:153], v[66:81]
	ds_read_b128 v[98:101], v223 offset:57344
	s_waitcnt lgkmcnt(0)
	v_mfma_f32_32x32x16_bf16 v[82:97], v[98:101], v[146:149], v[82:97]
	ds_read_b128 v[98:101], v224 offset:12288
	s_waitcnt lgkmcnt(0)
	v_mfma_f32_32x32x16_bf16 v[66:81], v[98:101], v[146:149], v[66:81]
	ds_read_b128 v[98:101], v217 offset:57472
	ds_read_b128 v[102:105], v218 offset:12416
	s_waitcnt lgkmcnt(1)
	v_mfma_f32_32x32x16_bf16 v[82:97], v[98:101], v[142:145], v[82:97]
	ds_read_b128 v[98:101], v219 offset:57472
	s_waitcnt lgkmcnt(1)
	v_mfma_f32_32x32x16_bf16 v[66:81], v[102:105], v[142:145], v[66:81]
	s_waitcnt lgkmcnt(0)
	v_mfma_f32_32x32x16_bf16 v[82:97], v[98:101], v[138:141], v[82:97]
	ds_read_b128 v[98:101], v220 offset:12416
	s_waitcnt lgkmcnt(0)
	v_mfma_f32_32x32x16_bf16 v[66:81], v[98:101], v[138:141], v[66:81]
	ds_read_b128 v[98:101], v221 offset:57472
	s_waitcnt lgkmcnt(0)
	v_mfma_f32_32x32x16_bf16 v[82:97], v[98:101], v[134:137], v[82:97]
	ds_read_b128 v[98:101], v222 offset:12416
	s_waitcnt lgkmcnt(0)
	v_mfma_f32_32x32x16_bf16 v[66:81], v[98:101], v[134:137], v[66:81]
	ds_read_b128 v[98:101], v223 offset:57472
	s_waitcnt lgkmcnt(0)
	v_mfma_f32_32x32x16_bf16 v[82:97], v[98:101], v[130:133], v[82:97]
	ds_read_b128 v[98:101], v224 offset:12416
	s_waitcnt lgkmcnt(0)
	v_mfma_f32_32x32x16_bf16 v[66:81], v[98:101], v[130:133], v[66:81]
	ds_read_b128 v[98:101], v217 offset:57600
	ds_read_b128 v[102:105], v218 offset:12544
	s_waitcnt lgkmcnt(1)
	v_mfma_f32_32x32x16_bf16 v[82:97], v[98:101], v[126:129], v[82:97]
	ds_read_b128 v[98:101], v219 offset:57600
	s_waitcnt lgkmcnt(1)
	v_mfma_f32_32x32x16_bf16 v[66:81], v[102:105], v[126:129], v[66:81]
	s_waitcnt lgkmcnt(0)
	v_mfma_f32_32x32x16_bf16 v[82:97], v[98:101], v[122:125], v[82:97]
	ds_read_b128 v[98:101], v220 offset:12544
	s_waitcnt lgkmcnt(0)
; #define PSUB_AT(k) do { if (PROBE_SUB == (k) && DK == PROBE_SUBDK) sacc = __builtin_amdgcn_readfirstlane(sacc + ((unsigned)__builtin_readcyclecounter() - ps_t0_)); } while (0)
; #define SBAR() __builtin_amdgcn_sched_barrier(0)
; #define SLOAD(k0) do { const unsigned so_k = (unsigned)((k0) * ldk) * 2u, so_v = (unsigned)((k0) * ldv) * 2u; \
;         _Pragma("unroll") for (int i = 0; i < KP; ++i) ks[i] = __builtin_amdgcn_raw_buffer_load_b128(krs, kgo[i], so_k, 0); \
;         vs0 = __builtin_amdgcn_raw_buffer_load_b128(vrs, vgo, so_v, 0); vs1 = __builtin_amdgcn_raw_buffer_load_b128(vrs, vgo + vstep, so_v, 0); } while (0)
; template <int DK, bool PF, bool EARLY, bool PFD = false> ...
;     ...
; #pragma unroll
;         for (int d0 = 0; d0 < NQ; ++d0) {
;             const bf16x8 b0 = *reinterpret_cast<const bf16x8*>(Kb + kra_(d0 & 3) + (d0 >> 2) * 128);
;             const bf16x8 b1 = *reinterpret_cast<const bf16x8*>(Kb + kra_(d0 & 3) + (d0 >> 2) * 128 + 32 * DK * 2);
;             p0 = __builtin_amdgcn_mfma_f32_32x32x16_bf16(b0, qr[d0], p0, 0, 0, 0);
;             p1 = __builtin_amdgcn_mfma_f32_32x32x16_bf16(b1, qr[d0], p1, 0, 0, 0);
;             if ((d0 & 3) == 3) SBAR();
;         }
;         PSUB_AT(1);
;         if (!EARLY && j + 1 < ntile) SLOAD((j + 1) * 64);
;         float ps = 0.f, ps1 = 0.f;
; #pragma unroll
;         for (int r = 0; r < 16; ++r) { p0[r] = __builtin_amdgcn_exp2f(p0[r]); p1[r] = __builtin_amdgcn_exp2f(p1[r]); ps += p0[r]; asm("" : "+v"(ps)); ps1 += p1[r]; asm("" : "+v"(ps1)); }
;         l_reg += ps + ps1;
;         bf16x8 pa0, pa1, pa2, pa3;
;     ...
;         PK4(p0, 0, pa0); PK4(p0, 8, pa1); PK4(p1, 0, pa2); PK4(p1, 8, pa3);
;     ...
;         PSUB_AT(2);
;         const int vb = vb0 + cur * SHM_V;
;         pv_one<0>(o[0], vb, pa0, pa1, pa2, pa3); pv_one<1>(o[1], vb, pa0, pa1, pa2, pa3); pv_one<2>(o[2], vb, pa0, pa1, pa2, pa3); pv_one<3>(o[3], vb, pa0, pa1, pa2, pa3);
	v_mfma_f32_32x32x16_bf16 v[66:81], v[98:101], v[122:125], v[66:81]
	ds_read_b128 v[98:101], v221 offset:57600
	s_waitcnt lgkmcnt(0)
	v_mfma_f32_32x32x16_bf16 v[82:97], v[98:101], v[118:121], v[82:97]
	ds_read_b128 v[98:101], v222 offset:12544
	s_waitcnt lgkmcnt(0)
	v_mfma_f32_32x32x16_bf16 v[66:81], v[98:101], v[118:121], v[66:81]
	ds_read_b128 v[98:101], v223 offset:57600
	s_waitcnt lgkmcnt(0)
	v_mfma_f32_32x32x16_bf16 v[82:97], v[98:101], v[114:117], v[82:97]
	ds_read_b128 v[98:101], v224 offset:12544
	s_waitcnt lgkmcnt(0)
	v_mfma_f32_32x32x16_bf16 v[66:81], v[98:101], v[114:117], v[66:81]
	s_nop 11
	v_exp_f32_e32 v98, v66
	v_exp_f32_e32 v82, v82
	v_exp_f32_e32 v67, v67
	v_exp_f32_e32 v83, v83
	v_add_f32_e32 v99, 0, v98
	v_exp_f32_e32 v100, v68
	v_add_f32_e32 v66, 0, v82
	v_exp_f32_e32 v84, v84
	v_add_f32_e32 v99, v67, v99
	v_exp_f32_e32 v85, v85
	v_add_f32_e32 v66, v83, v66
	v_add_f32_e32 v68, v100, v99
	v_exp_f32_e32 v99, v69
	v_exp_f32_e32 v86, v86
	v_add_f32_e32 v66, v84, v66
	v_exp_f32_e32 v101, v70
	v_exp_f32_e32 v70, v87
	v_add_f32_e32 v66, v85, v66
	v_add_f32_e32 v68, v99, v68
	v_exp_f32_e32 v87, v71
	v_exp_f32_e32 v71, v88
	v_add_f32_e32 v66, v86, v66
	v_add_f32_e32 v68, v101, v68
	v_exp_f32_e32 v88, v72
	v_exp_f32_e32 v72, v89
	v_add_f32_e32 v66, v70, v66
	v_add_f32_e32 v68, v87, v68
	v_exp_f32_e32 v89, v73
	v_exp_f32_e32 v73, v90
	v_add_f32_e32 v66, v71, v66
	v_add_f32_e32 v68, v88, v68
	v_exp_f32_e32 v90, v74
	v_exp_f32_e32 v74, v91
	v_add_f32_e32 v66, v72, v66
	v_add_f32_e32 v68, v89, v68
	v_exp_f32_e32 v91, v75
	v_exp_f32_e32 v75, v92
	v_add_f32_e32 v66, v73, v66
	v_add_f32_e32 v68, v90, v68
	v_exp_f32_e32 v92, v76
	v_exp_f32_e32 v76, v93
	v_add_f32_e32 v66, v74, v66
	v_add_f32_e32 v68, v91, v68
	v_exp_f32_e32 v93, v77
	v_exp_f32_e32 v77, v94
	v_add_f32_e32 v66, v75, v66
	v_add_f32_e32 v68, v92, v68
	v_exp_f32_e32 v94, v78
	v_exp_f32_e32 v78, v95
	v_add_f32_e32 v66, v76, v66
	v_add_f32_e32 v68, v93, v68
	v_exp_f32_e32 v95, v79
	v_exp_f32_e32 v79, v96
	v_add_f32_e32 v66, v77, v66
	v_add_f32_e32 v68, v94, v68
	v_exp_f32_e32 v96, v80
	v_exp_f32_e32 v80, v97
	v_add_f32_e32 v66, v78, v66
	v_add_f32_e32 v68, v95, v68
	v_exp_f32_e32 v97, v81
	s_nop 0
	v_add_f32_e32 v66, v79, v66
	v_add_f32_e32 v68, v96, v68
	s_nop 0
	v_add_f32_e32 v66, v80, v66
	v_add_f32_e32 v68, v97, v68
	s_nop 0
	v_add_f32_e32 v66, v66, v68
	v_cvt_pk_bf16_f32 v68, v82, v83
	v_cvt_pk_bf16_f32 v69, v84, v85
	v_cvt_pk_bf16_f32 v70, v86, v70
	v_cvt_pk_bf16_f32 v71, v71, v72
	v_cvt_pk_bf16_f32 v72, v73, v74
	v_cvt_pk_bf16_f32 v73, v75, v76
	v_cvt_pk_bf16_f32 v74, v77, v78
	v_cvt_pk_bf16_f32 v75, v79, v80
	v_cvt_pk_bf16_f32 v76, v98, v67
	v_cvt_pk_bf16_f32 v77, v100, v99
	v_cvt_pk_bf16_f32 v78, v101, v87
	v_cvt_pk_bf16_f32 v79, v88, v89
	v_cvt_pk_bf16_f32 v80, v90, v91
	v_cvt_pk_bf16_f32 v81, v92, v93
	v_cvt_pk_bf16_f32 v82, v94, v95
	v_cvt_pk_bf16_f32 v83, v96, v97
	ds_read_b64_tr_b16 v[84:85], v225 offset:0
	ds_read_b64_tr_b16 v[86:87], v225 offset:0x800
	ds_read_b64_tr_b16 v[88:89], v225 offset:0x1000
	ds_read_b64_tr_b16 v[90:91], v225 offset:0x1800
	ds_read_b64_tr_b16 v[92:93], v225 offset:0x2000
	ds_read_b64_tr_b16 v[94:95], v225 offset:0x2800
	ds_read_b64_tr_b16 v[96:97], v225 offset:0x3000
	ds_read_b64_tr_b16 v[98:99], v225 offset:0x3800
	s_waitcnt lgkmcnt(0)
	v_add_f32_e32 v66, v240, v66
	v_mfma_f32_32x32x16_bf16 v[2:17], v[68:71], v[84:87], v[2:17]
	ds_read_b64_tr_b16 v[84:85], v225 offset:0x200
	ds_read_b64_tr_b16 v[86:87], v225 offset:0xa00
	v_mfma_f32_32x32x16_bf16 v[2:17], v[72:75], v[88:91], v[2:17]
	ds_read_b64_tr_b16 v[88:89], v225 offset:0x1200
	ds_read_b64_tr_b16 v[90:91], v225 offset:0x1a00
	v_mfma_f32_32x32x16_bf16 v[2:17], v[76:79], v[92:95], v[2:17]
	ds_read_b64_tr_b16 v[92:93], v225 offset:0x2200
	ds_read_b64_tr_b16 v[94:95], v225 offset:0x2a00
	ds_read_b64_tr_b16 v[100:101], v225 offset:0x3200
	ds_read_b64_tr_b16 v[102:103], v225 offset:0x3a00
	s_waitcnt lgkmcnt(0)
	v_mfma_f32_32x32x16_bf16 v[2:17], v[80:83], v[96:99], v[2:17]
	v_mfma_f32_32x32x16_bf16 v[18:33], v[68:71], v[84:87], v[18:33]
	ds_read_b64_tr_b16 v[84:85], v225 offset:0x400
	ds_read_b64_tr_b16 v[86:87], v225 offset:0xc00
	v_mfma_f32_32x32x16_bf16 v[18:33], v[72:75], v[88:91], v[18:33]
	ds_read_b64_tr_b16 v[88:89], v225 offset:0x1400
	ds_read_b64_tr_b16 v[90:91], v225 offset:0x1c00
	v_mfma_f32_32x32x16_bf16 v[18:33], v[76:79], v[92:95], v[18:33]
	ds_read_b64_tr_b16 v[92:93], v225 offset:0x2400
	ds_read_b64_tr_b16 v[94:95], v225 offset:0x2c00
	ds_read_b64_tr_b16 v[96:97], v225 offset:0x3400
	ds_read_b64_tr_b16 v[98:99], v225 offset:0x3c00
	s_waitcnt lgkmcnt(0)
	v_mfma_f32_32x32x16_bf16 v[18:33], v[80:83], v[100:103], v[18:33]
	v_mfma_f32_32x32x16_bf16 v[34:49], v[68:71], v[84:87], v[34:49]
	ds_read_b64_tr_b16 v[84:85], v225 offset:0x600
	ds_read_b64_tr_b16 v[86:87], v225 offset:0xe00
	v_mfma_f32_32x32x16_bf16 v[34:49], v[72:75], v[88:91], v[34:49]
	ds_read_b64_tr_b16 v[88:89], v225 offset:0x1600
	ds_read_b64_tr_b16 v[90:91], v225 offset:0x1e00
	v_mfma_f32_32x32x16_bf16 v[34:49], v[76:79], v[92:95], v[34:49]
	ds_read_b64_tr_b16 v[92:93], v225 offset:0x2600
	ds_read_b64_tr_b16 v[94:95], v225 offset:0x2e00
	ds_read_b64_tr_b16 v[100:101], v225 offset:0x3600
	ds_read_b64_tr_b16 v[102:103], v225 offset:0x3e00
	s_waitcnt lgkmcnt(0)
	v_mfma_f32_32x32x16_bf16 v[34:49], v[80:83], v[96:99], v[34:49]
	v_mfma_f32_32x32x16_bf16 v[50:65], v[68:71], v[84:87], v[50:65]
	s_barrier
; __device__ __forceinline__ bf16 f2bf(float f) { unsigned u = __float_as_uint(f); return (bf16)((u + 0x7fffu + ((u >> 16) & 1u)) >> 16); }
; __device__ __forceinline__ int crow(int r, int hi) { return (r & 3) + 8 * (r >> 2) + 4 * hi; }
; __device__ __forceinline__ void row_recip(float l_reg, float* li_l  , int r32, int hi, float (&rli)[16]) {
;     { auto rr = __builtin_amdgcn_permlane32_swap(__float_as_uint(l_reg), __float_as_uint(l_reg), false, false); l_reg = __uint_as_float(rr[0]) + __uint_as_float(rr[1]); }
;     if (hi == 0) li_l[r32] = l_reg;
;     asm volatile("s_waitcnt lgkmcnt(0)" ::: "memory");
; #pragma unroll
;     for (int r = 0; r < 16; ++r) rli[r] = __builtin_amdgcn_rcpf(li_l[crow(r, hi)]);
; }
; __device__ __forceinline__ void mla_attn_unit(const Ptrs& P, unsigned char* lds, int b, int h, int qb, int ctxq, unsigned& sacc) {
;     ...
;     float rli[16]; row_recip(l_reg, (float*)(lds + ATT_SCR_OFF) + wid * 64, r32, hi, rli);
;     bf16* stg = (bf16*)lds + wid * 4096;
; #pragma unroll
;     for (int r = 0; r < 16; ++r) { const int orow = crow(r, hi);
; #pragma unroll
;         for (int d0 = 0; d0 < 4; ++d0) stg[orow * 128 + d0 * 32 + r32] = f2bf(o[d0][r] * rli[r]); }
	v_mfma_f32_32x32x16_bf16 v[50:65], v[72:75], v[88:91], v[50:65]
	v_mfma_f32_32x32x16_bf16 v[50:65], v[76:79], v[92:95], v[50:65]
	v_mfma_f32_32x32x16_bf16 v[50:65], v[80:83], v[100:103], v[50:65]
	s_setprio 0
	v_mov_b32_e32 v67, v66
	s_nop 1
	v_permlane32_swap_b32_e32 v66, v67
	s_and_saveexec_b64 s[8:9], s[6:7]
	v_add_f32_e32 v66, v66, v67
	ds_write_b32 v227, v66
	s_or_b64 exec, exec, s[8:9]
	s_waitcnt lgkmcnt(0)
	v_add_u32_e32 v74, v226, v228
	ds_read_b128 v[66:69], v74
	ds_read_b128 v[70:73], v74 offset:32
	s_lshl_b32 s38, s12, 1
	s_waitcnt lgkmcnt(1)
	v_rcp_f32_e32 v75, v66
	v_rcp_f32_e32 v76, v67
	v_rcp_f32_e32 v77, v68
	v_rcp_f32_e32 v78, v69
	v_mul_f32_e32 v2, v2, v75
	s_waitcnt lgkmcnt(0)
	v_rcp_f32_e32 v79, v70
	ds_read_b128 v[66:69], v74 offset:64
	v_rcp_f32_e32 v80, v71
	v_rcp_f32_e32 v81, v72
	v_rcp_f32_e32 v82, v73
	ds_read_b128 v[70:73], v74 offset:96
	v_bfe_u32 v74, v2, 16, 1
	v_add3_u32 v2, v2, v74, s46
	ds_write_b16_d16_hi v229, v2
	v_mul_f32_e32 v2, v18, v75
	v_bfe_u32 v18, v2, 16, 1
	v_add3_u32 v2, v2, v18, s46
	ds_write_b16_d16_hi v229, v2 offset:64
	v_mul_f32_e32 v2, v34, v75
	v_bfe_u32 v18, v2, 16, 1
	v_add3_u32 v2, v2, v18, s46
	ds_write_b16_d16_hi v229, v2 offset:128
	v_mul_f32_e32 v2, v50, v75
	v_bfe_u32 v18, v2, 16, 1
	v_add3_u32 v2, v2, v18, s46
	ds_write_b16_d16_hi v229, v2 offset:192
	v_mul_f32_e32 v2, v3, v76
	v_bfe_u32 v3, v2, 16, 1
	v_add3_u32 v2, v2, v3, s46
	ds_write_b16_d16_hi v229, v2 offset:256
	v_mul_f32_e32 v2, v19, v76
	v_bfe_u32 v3, v2, 16, 1
	v_add3_u32 v2, v2, v3, s46
	ds_write_b16_d16_hi v229, v2 offset:320
	v_mul_f32_e32 v2, v35, v76
	v_bfe_u32 v3, v2, 16, 1
	v_add3_u32 v2, v2, v3, s46
	ds_write_b16_d16_hi v229, v2 offset:384
	v_mul_f32_e32 v2, v51, v76
	v_bfe_u32 v3, v2, 16, 1
	v_add3_u32 v2, v2, v3, s46
	ds_write_b16_d16_hi v229, v2 offset:448
	v_mul_f32_e32 v2, v4, v77
	v_bfe_u32 v3, v2, 16, 1
	v_add3_u32 v2, v2, v3, s46
	ds_write_b16_d16_hi v229, v2 offset:512
	v_mul_f32_e32 v2, v20, v77
	v_bfe_u32 v3, v2, 16, 1
	v_add3_u32 v2, v2, v3, s46
	ds_write_b16_d16_hi v229, v2 offset:576
	v_mul_f32_e32 v2, v36, v77
	v_bfe_u32 v3, v2, 16, 1
	v_add3_u32 v2, v2, v3, s46
	ds_write_b16_d16_hi v229, v2 offset:640
	v_mul_f32_e32 v2, v52, v77
	v_bfe_u32 v3, v2, 16, 1
	v_add3_u32 v2, v2, v3, s46
	ds_write_b16_d16_hi v229, v2 offset:704
	v_mul_f32_e32 v2, v5, v78
	v_bfe_u32 v3, v2, 16, 1
	v_add3_u32 v2, v2, v3, s46
	ds_write_b16_d16_hi v229, v2 offset:768
	v_mul_f32_e32 v2, v21, v78
	v_bfe_u32 v3, v2, 16, 1
	v_add3_u32 v2, v2, v3, s46
	ds_write_b16_d16_hi v229, v2 offset:832
	v_mul_f32_e32 v2, v37, v78
	v_bfe_u32 v3, v2, 16, 1
	v_add3_u32 v2, v2, v3, s46
	ds_write_b16_d16_hi v229, v2 offset:896
	v_mul_f32_e32 v2, v53, v78
	v_bfe_u32 v3, v2, 16, 1
	v_add3_u32 v2, v2, v3, s46
	ds_write_b16_d16_hi v229, v2 offset:960
	v_mul_f32_e32 v2, v6, v79
	v_bfe_u32 v3, v2, 16, 1
	v_add3_u32 v2, v2, v3, s46
	ds_write_b16_d16_hi v229, v2 offset:2048
	v_mul_f32_e32 v2, v22, v79
	v_bfe_u32 v3, v2, 16, 1
	v_add3_u32 v2, v2, v3, s46
	ds_write_b16_d16_hi v229, v2 offset:2112
	v_mul_f32_e32 v2, v38, v79
	v_bfe_u32 v3, v2, 16, 1
	v_add3_u32 v2, v2, v3, s46
	ds_write_b16_d16_hi v229, v2 offset:2176
	v_mul_f32_e32 v2, v54, v79
	v_bfe_u32 v3, v2, 16, 1
	v_add3_u32 v2, v2, v3, s46
	ds_write_b16_d16_hi v229, v2 offset:2240
	v_mul_f32_e32 v2, v7, v80
	v_bfe_u32 v3, v2, 16, 1
	v_add3_u32 v2, v2, v3, s46
	ds_write_b16_d16_hi v229, v2 offset:2304
	v_mul_f32_e32 v2, v23, v80
	v_bfe_u32 v3, v2, 16, 1
	v_add3_u32 v2, v2, v3, s46
	ds_write_b16_d16_hi v229, v2 offset:2368
	v_mul_f32_e32 v2, v39, v80
	v_bfe_u32 v3, v2, 16, 1
	v_add3_u32 v2, v2, v3, s46
	ds_write_b16_d16_hi v229, v2 offset:2432
	v_mul_f32_e32 v2, v55, v80
	v_bfe_u32 v3, v2, 16, 1
	v_add3_u32 v2, v2, v3, s46
	ds_write_b16_d16_hi v229, v2 offset:2496
	v_mul_f32_e32 v2, v8, v81
	v_bfe_u32 v3, v2, 16, 1
	v_add3_u32 v2, v2, v3, s46
	ds_write_b16_d16_hi v229, v2 offset:2560
	v_mul_f32_e32 v2, v24, v81
	v_bfe_u32 v3, v2, 16, 1
	v_add3_u32 v2, v2, v3, s46
	ds_write_b16_d16_hi v229, v2 offset:2624
	v_mul_f32_e32 v2, v40, v81
	v_bfe_u32 v3, v2, 16, 1
	v_add3_u32 v2, v2, v3, s46
	ds_write_b16_d16_hi v229, v2 offset:2688
	v_mul_f32_e32 v2, v56, v81
	v_bfe_u32 v3, v2, 16, 1
	v_add3_u32 v2, v2, v3, s46
	ds_write_b16_d16_hi v229, v2 offset:2752
	v_mul_f32_e32 v2, v9, v82
	v_bfe_u32 v3, v2, 16, 1
	v_add3_u32 v2, v2, v3, s46
	ds_write_b16_d16_hi v229, v2 offset:2816
	v_mul_f32_e32 v2, v25, v82
	v_bfe_u32 v3, v2, 16, 1
	v_add3_u32 v2, v2, v3, s46
	ds_write_b16_d16_hi v229, v2 offset:2880
	v_mul_f32_e32 v2, v41, v82
	v_bfe_u32 v3, v2, 16, 1
	s_waitcnt lgkmcnt(14)
; __device__ __forceinline__ bf16 f2bf(float f) { unsigned u = __float_as_uint(f); return (bf16)((u + 0x7fffu + ((u >> 16) & 1u)) >> 16); }
; __device__ __forceinline__ int crow(int r, int hi) { return (r & 3) + 8 * (r >> 2) + 4 * hi; }
; __device__ __forceinline__ void mla_attn_unit(const Ptrs& P, unsigned char* lds, int b, int h, int qb, int ctxq, unsigned& sacc) {
;     ...
;     for (int r = 0; r < 16; ++r) { const int orow = crow(r, hi);
; #pragma unroll
;         for (int d0 = 0; d0 < 4; ++d0) stg[orow * 128 + d0 * 32 + r32] = f2bf(o[d0][r] * rli[r]); }
;     asm volatile("s_waitcnt lgkmcnt(0)" ::: "memory");
;     bf16* mix = (bf16*)(P.ws + WS_MIX) + u0 * D + 512 + h * 128;
; #pragma unroll
;     for (int i = 0; i < 8; ++i) { const int row = i * 4 + (lane >> 4), ch = lane & 15; const u32x4 v = *(const u32x4*)(stg + row * 128 + ch * 8); *(u32x4*)(mix + (size_t)row * D + ch * 8) = v; }
;     asm volatile("s_waitcnt lgkmcnt(0)" ::: "memory");
;     __syncthreads();
	v_rcp_f32_e32 v66, v66
	v_add3_u32 v2, v2, v3, s46
	ds_write_b16_d16_hi v229, v2 offset:2944
	v_mul_f32_e32 v2, v57, v82
	v_bfe_u32 v3, v2, 16, 1
	v_add3_u32 v2, v2, v3, s46
	ds_write_b16_d16_hi v229, v2 offset:3008
	v_mul_f32_e32 v2, v10, v66
	v_bfe_u32 v3, v2, 16, 1
	v_add3_u32 v2, v2, v3, s46
	ds_write_b16_d16_hi v229, v2 offset:4096
	v_mul_f32_e32 v2, v26, v66
	v_bfe_u32 v3, v2, 16, 1
	v_add3_u32 v2, v2, v3, s46
	ds_write_b16_d16_hi v229, v2 offset:4160
	v_mul_f32_e32 v2, v42, v66
	v_bfe_u32 v3, v2, 16, 1
	v_rcp_f32_e32 v67, v67
	v_add3_u32 v2, v2, v3, s46
	ds_write_b16_d16_hi v229, v2 offset:4224
	v_mul_f32_e32 v2, v58, v66
	v_bfe_u32 v3, v2, 16, 1
	v_add3_u32 v2, v2, v3, s46
	ds_write_b16_d16_hi v229, v2 offset:4288
	v_mul_f32_e32 v2, v11, v67
	v_bfe_u32 v3, v2, 16, 1
	v_add3_u32 v2, v2, v3, s46
	ds_write_b16_d16_hi v229, v2 offset:4352
	v_mul_f32_e32 v2, v27, v67
	v_bfe_u32 v3, v2, 16, 1
	v_add3_u32 v2, v2, v3, s46
	ds_write_b16_d16_hi v229, v2 offset:4416
	v_mul_f32_e32 v2, v43, v67
	v_bfe_u32 v3, v2, 16, 1
	v_rcp_f32_e32 v68, v68
	v_add3_u32 v2, v2, v3, s46
	ds_write_b16_d16_hi v229, v2 offset:4480
	v_mul_f32_e32 v2, v59, v67
	v_bfe_u32 v3, v2, 16, 1
	v_add3_u32 v2, v2, v3, s46
	ds_write_b16_d16_hi v229, v2 offset:4544
	v_mul_f32_e32 v2, v12, v68
	v_bfe_u32 v3, v2, 16, 1
	v_add3_u32 v2, v2, v3, s46
	ds_write_b16_d16_hi v229, v2 offset:4608
	v_mul_f32_e32 v2, v28, v68
	v_bfe_u32 v3, v2, 16, 1
	v_add3_u32 v2, v2, v3, s46
	ds_write_b16_d16_hi v229, v2 offset:4672
	v_mul_f32_e32 v2, v44, v68
	v_bfe_u32 v3, v2, 16, 1
	v_rcp_f32_e32 v69, v69
	v_add3_u32 v2, v2, v3, s46
	ds_write_b16_d16_hi v229, v2 offset:4736
	v_mul_f32_e32 v2, v60, v68
	v_bfe_u32 v3, v2, 16, 1
	v_add3_u32 v2, v2, v3, s46
	ds_write_b16_d16_hi v229, v2 offset:4800
	v_mul_f32_e32 v2, v13, v69
	v_bfe_u32 v3, v2, 16, 1
	v_add3_u32 v2, v2, v3, s46
	ds_write_b16_d16_hi v229, v2 offset:4864
	v_mul_f32_e32 v2, v29, v69
	v_bfe_u32 v3, v2, 16, 1
	v_add3_u32 v2, v2, v3, s46
	ds_write_b16_d16_hi v229, v2 offset:4928
	v_mul_f32_e32 v2, v45, v69
	v_bfe_u32 v3, v2, 16, 1
	v_rcp_f32_e32 v70, v70
	v_add3_u32 v2, v2, v3, s46
	ds_write_b16_d16_hi v229, v2 offset:4992
	v_mul_f32_e32 v2, v61, v69
	v_bfe_u32 v3, v2, 16, 1
	v_add3_u32 v2, v2, v3, s46
	ds_write_b16_d16_hi v229, v2 offset:5056
	v_mul_f32_e32 v2, v14, v70
	v_bfe_u32 v3, v2, 16, 1
	v_add3_u32 v2, v2, v3, s46
	ds_write_b16_d16_hi v229, v2 offset:6144
	v_mul_f32_e32 v2, v30, v70
	v_bfe_u32 v3, v2, 16, 1
	v_add3_u32 v2, v2, v3, s46
	ds_write_b16_d16_hi v229, v2 offset:6208
	v_mul_f32_e32 v2, v46, v70
	v_bfe_u32 v3, v2, 16, 1
	v_rcp_f32_e32 v71, v71
	v_add3_u32 v2, v2, v3, s46
	ds_write_b16_d16_hi v229, v2 offset:6272
	v_mul_f32_e32 v2, v62, v70
	v_bfe_u32 v3, v2, 16, 1
	v_add3_u32 v2, v2, v3, s46
	ds_write_b16_d16_hi v229, v2 offset:6336
	v_mul_f32_e32 v2, v15, v71
	v_bfe_u32 v3, v2, 16, 1
	v_add3_u32 v2, v2, v3, s46
	ds_write_b16_d16_hi v229, v2 offset:6400
	v_mul_f32_e32 v2, v31, v71
	v_bfe_u32 v3, v2, 16, 1
	v_add3_u32 v2, v2, v3, s46
	ds_write_b16_d16_hi v229, v2 offset:6464
	v_mul_f32_e32 v2, v47, v71
	v_bfe_u32 v3, v2, 16, 1
	v_rcp_f32_e32 v72, v72
	v_add3_u32 v2, v2, v3, s46
	ds_write_b16_d16_hi v229, v2 offset:6528
	v_mul_f32_e32 v2, v63, v71
	v_bfe_u32 v3, v2, 16, 1
	v_add3_u32 v2, v2, v3, s46
	ds_write_b16_d16_hi v229, v2 offset:6592
	v_mul_f32_e32 v2, v16, v72
	v_bfe_u32 v3, v2, 16, 1
	v_add3_u32 v2, v2, v3, s46
	ds_write_b16_d16_hi v229, v2 offset:6656
	v_mul_f32_e32 v2, v32, v72
	v_bfe_u32 v3, v2, 16, 1
	v_add3_u32 v2, v2, v3, s46
	ds_write_b16_d16_hi v229, v2 offset:6720
	v_mul_f32_e32 v2, v48, v72
	v_bfe_u32 v3, v2, 16, 1
	v_rcp_f32_e32 v73, v73
	v_add3_u32 v2, v2, v3, s46
	ds_write_b16_d16_hi v229, v2 offset:6784
	v_mul_f32_e32 v2, v64, v72
	v_bfe_u32 v3, v2, 16, 1
	v_add3_u32 v2, v2, v3, s46
	ds_write_b16_d16_hi v229, v2 offset:6848
	v_mul_f32_e32 v2, v17, v73
	v_bfe_u32 v3, v2, 16, 1
	v_add3_u32 v2, v2, v3, s46
	ds_write_b16_d16_hi v229, v2 offset:6912
	v_mul_f32_e32 v2, v33, v73
	v_bfe_u32 v3, v2, 16, 1
	v_add3_u32 v2, v2, v3, s46
	ds_write_b16_d16_hi v229, v2 offset:6976
	v_mul_f32_e32 v2, v49, v73
	v_bfe_u32 v3, v2, 16, 1
	v_add3_u32 v2, v2, v3, s46
	ds_write_b16_d16_hi v229, v2 offset:7040
	v_mul_f32_e32 v2, v65, v73
	v_bfe_u32 v3, v2, 16, 1
	v_add3_u32 v2, v2, v3, s46
	ds_write_b16_d16_hi v229, v2 offset:7104
	v_lshlrev_b64 v[2:3], 11, v[212:213]
	v_lshl_add_u64 v[2:3], s[78:79], 0, v[2:3]
	v_lshl_add_u64 v[2:3], v[2:3], 0, s[38:39]
	v_lshlrev_b32_e32 v4, 1, v192
	v_mov_b32_e32 v5, v189
	v_lshl_add_u64 v[2:3], v[2:3], 0, v[4:5]
	s_waitcnt lgkmcnt(0)
	v_lshl_add_u64 v[10:11], v[2:3], 0, s[40:41]
	v_add_u32_e32 v2, v230, v231
	ds_read_b128 v[2:5], v2
	v_lshlrev_b32_e32 v6, 1, v194
	v_mov_b32_e32 v7, v189
	v_lshl_add_u64 v[12:13], v[10:11], 0, v[6:7]
	v_add_u32_e32 v6, v230, v232
	ds_read_b128 v[6:9], v6
	s_waitcnt lgkmcnt(1)
	global_store_dwordx4 v[12:13], v[2:5], off
	s_nop 1
	v_lshlrev_b32_e32 v2, 1, v196
	v_mov_b32_e32 v3, v189
	v_lshl_add_u64 v[2:3], v[10:11], 0, v[2:3]
	s_waitcnt lgkmcnt(0)
	global_store_dwordx4 v[2:3], v[6:9], off
	v_add_u32_e32 v2, v230, v233
	ds_read_b128 v[2:5], v2
	v_lshlrev_b32_e32 v6, 1, v198
	v_mov_b32_e32 v7, v189
	v_lshl_add_u64 v[12:13], v[10:11], 0, v[6:7]
	v_add_u32_e32 v6, v230, v234
	ds_read_b128 v[6:9], v6
	s_waitcnt lgkmcnt(1)
	global_store_dwordx4 v[12:13], v[2:5], off
	s_nop 1
	v_lshlrev_b32_e32 v2, 1, v200
	v_mov_b32_e32 v3, v189
	v_lshl_add_u64 v[2:3], v[10:11], 0, v[2:3]
	s_waitcnt lgkmcnt(0)
	global_store_dwordx4 v[2:3], v[6:9], off
	v_add_u32_e32 v2, v230, v235
	ds_read_b128 v[2:5], v2
	v_lshlrev_b32_e32 v6, 1, v202
	v_mov_b32_e32 v7, v189
	v_lshl_add_u64 v[12:13], v[10:11], 0, v[6:7]
	v_add_u32_e32 v6, v230, v236
	ds_read_b128 v[6:9], v6
	s_waitcnt lgkmcnt(1)
	global_store_dwordx4 v[12:13], v[2:5], off
	s_nop 1
	v_lshlrev_b32_e32 v2, 1, v204
	v_mov_b32_e32 v3, v189
	v_lshl_add_u64 v[2:3], v[10:11], 0, v[2:3]
	s_waitcnt lgkmcnt(0)
	global_store_dwordx4 v[2:3], v[6:9], off
	v_add_u32_e32 v2, v230, v237
	ds_read_b128 v[2:5], v2
	v_lshlrev_b32_e32 v6, 1, v206
	v_mov_b32_e32 v7, v189
	v_lshl_add_u64 v[12:13], v[10:11], 0, v[6:7]
	v_add_u32_e32 v6, v230, v238
	ds_read_b128 v[6:9], v6
	s_waitcnt lgkmcnt(1)
	global_store_dwordx4 v[12:13], v[2:5], off
	s_nop 1
	v_lshlrev_b32_e32 v2, 1, v208
	v_mov_b32_e32 v3, v189
	v_lshl_add_u64 v[2:3], v[10:11], 0, v[2:3]
	s_waitcnt lgkmcnt(0)
	global_store_dwordx4 v[2:3], v[6:9], off
	s_waitcnt lgkmcnt(0)
	s_barrier
	s_branch .LBB0_1187

; #define PSUB_AT(k) do { if (PROBE_SUB == (k) && DK == PROBE_SUBDK) sacc = __builtin_amdgcn_readfirstlane(sacc + ((unsigned)__builtin_readcyclecounter() - ps_t0_)); } while (0)
; #define SBAR() __builtin_amdgcn_sched_barrier(0)
; #define SLOAD(k0) do { const unsigned so_k = (unsigned)((k0) * ldk) * 2u, so_v = (unsigned)((k0) * ldv) * 2u; \
;         _Pragma("unroll") for (int i = 0; i < KP; ++i) ks[i] = __builtin_amdgcn_raw_buffer_load_b128(krs, kgo[i], so_k, 0); \
;         vs0 = __builtin_amdgcn_raw_buffer_load_b128(vrs, vgo, so_v, 0); vs1 = __builtin_amdgcn_raw_buffer_load_b128(vrs, vgo + vstep, so_v, 0); } while (0)
; template <int DK, bool PF, bool EARLY, bool PFD = false> ...
;     ...
;         if (EARLY && j + 1 < ntile) SLOAD((j + 1) * 64);
;         f32x16 p0, p1;
; #pragma unroll
;         for (int r = 0; r < 16; ++r) { p0[r] = negM; p1[r] = negM; }
;         const char* Kb = K_lds + cur * SHM_K;
; #pragma unroll
;         for (int d0 = 0; d0 < NQ; ++d0) {
;             const bf16x8 b0 = *reinterpret_cast<const bf16x8*>(Kb + kra_(d0 & 3) + (d0 >> 2) * 128);
;             const bf16x8 b1 = *reinterpret_cast<const bf16x8*>(Kb + kra_(d0 & 3) + (d0 >> 2) * 128 + 32 * DK * 2);
;             p0 = __builtin_amdgcn_mfma_f32_32x32x16_bf16(b0, qr[d0], p0, 0, 0, 0);
;             p1 = __builtin_amdgcn_mfma_f32_32x32x16_bf16(b1, qr[d0], p1, 0, 0, 0);
;             if ((d0 & 3) == 3) SBAR();
;         }
;         PSUB_AT(1);
;         if (!EARLY && j + 1 < ntile) SLOAD((j + 1) * 64);
;         float ps = 0.f, ps1 = 0.f;
; #pragma unroll
;         for (int r = 0; r < 16; ++r) { p0[r] = __builtin_amdgcn_exp2f(p0[r]); p1[r] = __builtin_amdgcn_exp2f(p1[r]); ps += p0[r]; asm("" : "+v"(ps)); ps1 += p1[r]; asm("" : "+v"(ps1)); }
;         l_reg += ps + ps1;
;         bf16x8 pa0, pa1, pa2, pa3;
;     ...
;         PK4(p0, 0, pa0); PK4(p0, 8, pa1); PK4(p1, 0, pa2); PK4(p1, 8, pa3);
;     ...
;         PSUB_AT(2);
;         const int vb = vb0 + cur * SHM_V;
;         pv_one<0>(o[0], vb, pa0, pa1, pa2, pa3); pv_one<1>(o[1], vb, pa0, pa1, pa2, pa3); pv_one<2>(o[2], vb, pa0, pa1, pa2, pa3); pv_one<3>(o[3], vb, pa0, pa1, pa2, pa3);
.LBB0_1200:
	s_and_b32 s23, s19, 1
	s_mul_i32 s24, s23, 0x6000
	v_add_u32_e32 v250, s24, v207
	v_add_u32_e32 v251, v250, v201
	v_add_u32_e32 v252, v250, v214
	v_add_u32_e32 v253, v250, v215
	v_add_u32_e32 v245, v250, v216
	ds_read_b128 v[162:165], v251 offset:32768
	ds_read_b128 v[166:169], v251 offset:45056
	ds_read_b128 v[170:173], v252 offset:32768
	ds_read_b128 v[174:177], v252 offset:45056
	ds_read_b128 v[178:181], v253 offset:32768
	ds_read_b128 v[246:249], v253 offset:45056
	s_waitcnt lgkmcnt(5)
	v_mfma_f32_32x32x16_bf16 v[98:113], v[162:165], v[158:161], v[66:81]
	ds_read_b128 v[162:165], v245 offset:32768
	s_waitcnt lgkmcnt(5)
	v_mfma_f32_32x32x16_bf16 v[82:97], v[166:169], v[158:161], v[66:81]
	ds_read_b128 v[166:169], v245 offset:45056
	s_waitcnt lgkmcnt(5)
	v_mfma_f32_32x32x16_bf16 v[98:113], v[170:173], v[154:157], v[98:113]
	ds_read_b128 v[170:173], v251 offset:32896
	s_waitcnt lgkmcnt(5)
	v_mfma_f32_32x32x16_bf16 v[82:97], v[174:177], v[154:157], v[82:97]
	ds_read_b128 v[174:177], v251 offset:45184
	s_waitcnt lgkmcnt(5)
	v_mfma_f32_32x32x16_bf16 v[98:113], v[178:181], v[150:153], v[98:113]
	ds_read_b128 v[178:181], v252 offset:32896
	s_waitcnt lgkmcnt(5)
	v_mfma_f32_32x32x16_bf16 v[82:97], v[246:249], v[150:153], v[82:97]
	ds_read_b128 v[246:249], v252 offset:45184
	s_waitcnt lgkmcnt(5)
	v_mfma_f32_32x32x16_bf16 v[98:113], v[162:165], v[146:149], v[98:113]
	ds_read_b128 v[162:165], v253 offset:32896
	s_waitcnt lgkmcnt(5)
	v_mfma_f32_32x32x16_bf16 v[82:97], v[166:169], v[146:149], v[82:97]
	ds_read_b128 v[166:169], v253 offset:45184
	s_waitcnt lgkmcnt(5)
	v_mfma_f32_32x32x16_bf16 v[98:113], v[170:173], v[142:145], v[98:113]
	ds_read_b128 v[170:173], v245 offset:32896
	s_waitcnt lgkmcnt(5)
	v_mfma_f32_32x32x16_bf16 v[82:97], v[174:177], v[142:145], v[82:97]
	ds_read_b128 v[174:177], v245 offset:45184
	s_waitcnt lgkmcnt(5)
	v_mfma_f32_32x32x16_bf16 v[98:113], v[178:181], v[138:141], v[98:113]
	ds_read_b128 v[178:181], v251 offset:33024
	s_waitcnt lgkmcnt(5)
	v_mfma_f32_32x32x16_bf16 v[82:97], v[246:249], v[138:141], v[82:97]
	ds_read_b128 v[246:249], v251 offset:45312
	s_waitcnt lgkmcnt(5)
	v_mfma_f32_32x32x16_bf16 v[98:113], v[162:165], v[134:137], v[98:113]
	ds_read_b128 v[162:165], v252 offset:33024
	s_waitcnt lgkmcnt(5)
	v_mfma_f32_32x32x16_bf16 v[82:97], v[166:169], v[134:137], v[82:97]
	ds_read_b128 v[166:169], v252 offset:45312
	s_waitcnt lgkmcnt(5)
	v_mfma_f32_32x32x16_bf16 v[98:113], v[170:173], v[130:133], v[98:113]
	ds_read_b128 v[170:173], v253 offset:33024
	s_waitcnt lgkmcnt(5)
	v_mfma_f32_32x32x16_bf16 v[82:97], v[174:177], v[130:133], v[82:97]
	ds_read_b128 v[174:177], v253 offset:45312
	s_waitcnt lgkmcnt(5)
	v_mfma_f32_32x32x16_bf16 v[98:113], v[178:181], v[126:129], v[98:113]
	ds_read_b128 v[178:181], v245 offset:33024
	s_waitcnt lgkmcnt(5)
	v_mfma_f32_32x32x16_bf16 v[82:97], v[246:249], v[126:129], v[82:97]
	ds_read_b128 v[246:249], v245 offset:45312
	s_waitcnt lgkmcnt(5)
	v_mfma_f32_32x32x16_bf16 v[98:113], v[162:165], v[122:125], v[98:113]
	s_waitcnt lgkmcnt(4)
	v_mfma_f32_32x32x16_bf16 v[82:97], v[166:169], v[122:125], v[82:97]
	s_waitcnt lgkmcnt(3)
	v_mfma_f32_32x32x16_bf16 v[98:113], v[170:173], v[118:121], v[98:113]
	s_waitcnt lgkmcnt(2)
	v_mfma_f32_32x32x16_bf16 v[82:97], v[174:177], v[118:121], v[82:97]
	s_waitcnt lgkmcnt(1)
	v_mfma_f32_32x32x16_bf16 v[98:113], v[178:181], v[114:117], v[98:113]
	s_waitcnt lgkmcnt(0)
	v_mfma_f32_32x32x16_bf16 v[82:97], v[246:249], v[114:117], v[82:97]
	buffer_load_dwordx4 v[166:169], v185, s[8:11], s20 offen
	buffer_load_dwordx4 v[162:165], v191, s[8:11], s20 offen
	buffer_load_dwordx4 v[178:181], v195, s[8:11], s20 offen
	buffer_load_dwordx4 v[170:173], v199, s[12:15], s21 offen
	buffer_load_dwordx4 v[174:177], v203, s[12:15], s21 offen
	s_lshl_b32 s33, s23, 14
	v_add_u32_e32 v245, s33, v209
	ds_read_b64_tr_b16 v[246:247], v245 offset:0x0
	ds_read_b64_tr_b16 v[248:249], v245 offset:0x800
	ds_read_b64_tr_b16 v[250:251], v245 offset:0x1000
	ds_read_b64_tr_b16 v[252:253], v245 offset:0x1800
	s_nop 1
	v_exp_f32_e32 v240, v82
	v_exp_f32_e32 v98, v98
	v_exp_f32_e32 v242, v83
	v_exp_f32_e32 v99, v99
	v_add_f32_e32 v241, 0, v240
	v_add_f32_e32 v82, 0, v98
	v_exp_f32_e32 v83, v100
	v_add_f32_e32 v100, v242, v241
	v_exp_f32_e32 v241, v84
	v_add_f32_e32 v82, v99, v82
	v_exp_f32_e32 v84, v101
	v_exp_f32_e32 v101, v85
	v_add_f32_e32 v82, v83, v82
	v_exp_f32_e32 v85, v102
	v_add_f32_e32 v100, v241, v100
	v_exp_f32_e32 v102, v86
	v_add_f32_e32 v82, v84, v82
	v_exp_f32_e32 v86, v103
	v_add_f32_e32 v100, v101, v100
	v_exp_f32_e32 v103, v87
	v_add_f32_e32 v82, v85, v82
	v_exp_f32_e32 v87, v104
	v_add_f32_e32 v100, v102, v100
	v_exp_f32_e32 v104, v88
	v_add_f32_e32 v82, v86, v82
	v_exp_f32_e32 v88, v105
	v_add_f32_e32 v100, v103, v100
	v_exp_f32_e32 v105, v89
	v_add_f32_e32 v82, v87, v82
	v_exp_f32_e32 v89, v106
	v_add_f32_e32 v100, v104, v100
	v_exp_f32_e32 v106, v90
	v_add_f32_e32 v82, v88, v82
	v_exp_f32_e32 v90, v107
	v_add_f32_e32 v100, v105, v100
	v_exp_f32_e32 v107, v91
	v_add_f32_e32 v82, v89, v82
	v_exp_f32_e32 v91, v108
	v_add_f32_e32 v100, v106, v100
	v_exp_f32_e32 v108, v92
	v_add_f32_e32 v82, v90, v82
	v_exp_f32_e32 v92, v109
	v_add_f32_e32 v100, v107, v100
	v_exp_f32_e32 v109, v93
	v_add_f32_e32 v82, v91, v82
	v_exp_f32_e32 v93, v110
	v_add_f32_e32 v100, v108, v100
	v_exp_f32_e32 v110, v94
	v_add_f32_e32 v82, v92, v82
	v_exp_f32_e32 v94, v111
	v_add_f32_e32 v100, v109, v100
	v_exp_f32_e32 v111, v95
	v_add_f32_e32 v82, v93, v82
	v_exp_f32_e32 v95, v112
	v_add_f32_e32 v100, v110, v100
	v_exp_f32_e32 v112, v96
	v_add_f32_e32 v82, v94, v82
	v_exp_f32_e32 v96, v113
	v_add_f32_e32 v100, v111, v100
	v_exp_f32_e32 v97, v97
	v_add_f32_e32 v82, v95, v82
	v_add_f32_e32 v100, v112, v100
	v_add_f32_e32 v82, v96, v82
	v_add_f32_e32 v100, v97, v100
	s_lshl_b32 s24, s23, 14
	v_add_f32_e32 v82, v82, v100
	v_add_f32_e32 v188, v188, v82
	v_cvt_pk_bf16_f32 v82, v98, v99
	v_cvt_pk_bf16_f32 v83, v83, v84
	v_cvt_pk_bf16_f32 v84, v85, v86
	v_cvt_pk_bf16_f32 v85, v87, v88
	v_cvt_pk_bf16_f32 v86, v89, v90
	v_cvt_pk_bf16_f32 v87, v91, v92
	v_cvt_pk_bf16_f32 v88, v93, v94
	v_cvt_pk_bf16_f32 v89, v95, v96
	v_cvt_pk_bf16_f32 v90, v240, v242
	v_cvt_pk_bf16_f32 v91, v241, v101
	v_cvt_pk_bf16_f32 v92, v102, v103
	v_cvt_pk_bf16_f32 v93, v104, v105
	v_cvt_pk_bf16_f32 v94, v106, v107
	v_cvt_pk_bf16_f32 v95, v108, v109
	v_cvt_pk_bf16_f32 v96, v110, v111
	v_cvt_pk_bf16_f32 v97, v112, v97
	v_add_u32_e32 v244, s24, v209
	ds_read_b64_tr_b16 v[106:107], v244 offset:0x2000
	ds_read_b64_tr_b16 v[108:109], v244 offset:0x2800
	ds_read_b64_tr_b16 v[110:111], v244 offset:0x3000
	ds_read_b64_tr_b16 v[112:113], v244 offset:0x3800
	s_add_i32 s19, s19, 1
	s_waitcnt lgkmcnt(4)
; #define PSUB_AT(k) do { if (PROBE_SUB == (k) && DK == PROBE_SUBDK) sacc = __builtin_amdgcn_readfirstlane(sacc + ((unsigned)__builtin_readcyclecounter() - ps_t0_)); } while (0)
; #define SBAR() __builtin_amdgcn_sched_barrier(0)
; #define SWRITE(b) do { _Pragma("unroll") for (int i = 0; i < KP; ++i) *reinterpret_cast<u32x4*>(K_lds + (b) * SHM_K + kst[i]) = ks[i]; \
;         *reinterpret_cast<u32x4*>(V_lds + (b) * SHM_V + vst0) = vs0; *reinterpret_cast<u32x4*>(V_lds + (b) * SHM_V + vst0 + vst1d) = vs1; } while (0)
; template <int DK, bool PF, bool EARLY, bool PFD = false> ...
;     ...
;         const char* Kb = K_lds + cur * SHM_K;
; #pragma unroll
;         for (int d0 = 0; d0 < NQ; ++d0) {
;             const bf16x8 b0 = *reinterpret_cast<const bf16x8*>(Kb + kra_(d0 & 3) + (d0 >> 2) * 128);
;             const bf16x8 b1 = *reinterpret_cast<const bf16x8*>(Kb + kra_(d0 & 3) + (d0 >> 2) * 128 + 32 * DK * 2);
;             p0 = __builtin_amdgcn_mfma_f32_32x32x16_bf16(b0, qr[d0], p0, 0, 0, 0);
;             p1 = __builtin_amdgcn_mfma_f32_32x32x16_bf16(b1, qr[d0], p1, 0, 0, 0);
;             if ((d0 & 3) == 3) SBAR();
;         }
;     ...
;         const int vb = vb0 + cur * SHM_V;
;         pv_one<0>(o[0], vb, pa0, pa1, pa2, pa3); pv_one<1>(o[1], vb, pa0, pa1, pa2, pa3); pv_one<2>(o[2], vb, pa0, pa1, pa2, pa3); pv_one<3>(o[3], vb, pa0, pa1, pa2, pa3);
;         PSUB_AT(3);
;         if (j + 1 < ntile) SWRITE(cur ^ 1);
;         if (j + 3 < ntile) PREFETCH(j + 3);
;         __syncthreads();
	v_mfma_f32_32x32x16_bf16 v[2:17], v[82:85], v[246:249], v[2:17]
	ds_read_b64_tr_b16 v[98:99], v244 offset:0x200
	ds_read_b64_tr_b16 v[100:101], v244 offset:0xa00
	v_mfma_f32_32x32x16_bf16 v[2:17], v[86:89], v[250:253], v[2:17]
	ds_read_b64_tr_b16 v[102:103], v244 offset:0x1200
	ds_read_b64_tr_b16 v[104:105], v244 offset:0x1a00
	s_waitcnt lgkmcnt(6)
	v_mfma_f32_32x32x16_bf16 v[2:17], v[90:93], v[106:109], v[2:17]
	ds_read_b64_tr_b16 v[106:107], v244 offset:0x2200
	ds_read_b64_tr_b16 v[108:109], v244 offset:0x2a00
	ds_read_b64_tr_b16 v[240:241], v244 offset:0x3200
	ds_read_b64_tr_b16 v[242:243], v244 offset:0x3a00
	s_waitcnt lgkmcnt(8)
	v_mfma_f32_32x32x16_bf16 v[2:17], v[94:97], v[110:113], v[2:17]
	s_waitcnt lgkmcnt(6)
	v_mfma_f32_32x32x16_bf16 v[18:33], v[82:85], v[98:101], v[18:33]
	ds_read_b64_tr_b16 v[98:99], v244 offset:0x400
	ds_read_b64_tr_b16 v[100:101], v244 offset:0xc00
	s_waitcnt lgkmcnt(6)
	v_mfma_f32_32x32x16_bf16 v[18:33], v[86:89], v[102:105], v[18:33]
	ds_read_b64_tr_b16 v[102:103], v244 offset:0x1400
	ds_read_b64_tr_b16 v[104:105], v244 offset:0x1c00
	s_waitcnt lgkmcnt(6)
	v_mfma_f32_32x32x16_bf16 v[18:33], v[90:93], v[106:109], v[18:33]
	ds_read_b64_tr_b16 v[106:107], v244 offset:0x2400
	ds_read_b64_tr_b16 v[108:109], v244 offset:0x2c00
	ds_read_b64_tr_b16 v[110:111], v244 offset:0x3400
	ds_read_b64_tr_b16 v[112:113], v244 offset:0x3c00
	s_waitcnt lgkmcnt(8)
	v_mfma_f32_32x32x16_bf16 v[18:33], v[94:97], v[240:243], v[18:33]
	s_waitcnt lgkmcnt(6)
	v_mfma_f32_32x32x16_bf16 v[34:49], v[82:85], v[98:101], v[34:49]
	ds_read_b64_tr_b16 v[98:99], v244 offset:0x600
	ds_read_b64_tr_b16 v[100:101], v244 offset:0xe00
	s_waitcnt lgkmcnt(6)
	v_mfma_f32_32x32x16_bf16 v[34:49], v[86:89], v[102:105], v[34:49]
	ds_read_b64_tr_b16 v[102:103], v244 offset:0x1600
	ds_read_b64_tr_b16 v[104:105], v244 offset:0x1e00
	s_waitcnt lgkmcnt(6)
	v_mfma_f32_32x32x16_bf16 v[34:49], v[90:93], v[106:109], v[34:49]
	ds_read_b64_tr_b16 v[106:107], v244 offset:0x2600
	ds_read_b64_tr_b16 v[108:109], v244 offset:0x2e00
	ds_read_b64_tr_b16 v[240:241], v244 offset:0x3600
	ds_read_b64_tr_b16 v[242:243], v244 offset:0x3e00
	s_waitcnt lgkmcnt(8)
	v_mfma_f32_32x32x16_bf16 v[34:49], v[94:97], v[110:113], v[34:49]
	s_waitcnt lgkmcnt(6)
	v_mfma_f32_32x32x16_bf16 v[50:65], v[82:85], v[98:101], v[50:65]
	s_waitcnt lgkmcnt(0)
	s_xor_b32 s23, s23, 1
	s_mulk_i32 s23, 0x6000
	s_add_i32 s23, s23, 0
	v_add_u32_e32 v82, s23, v187
	s_waitcnt vmcnt(4)
	ds_write_b128 v82, v[166:169] offset:32768
	v_add_u32_e32 v82, s23, v193
	s_waitcnt vmcnt(3)
	ds_write_b128 v82, v[162:165] offset:32768
	v_mfma_f32_32x32x16_bf16 v[50:65], v[86:89], v[102:105], v[50:65]
	v_add_u32_e32 v82, s23, v197
	s_xor_b32 s23, s24, 0x4000
	s_add_i32 s20, s20, 0x18000
	s_add_i32 s21, s21, 0x10000
	v_add_u32_e32 v83, s23, v205
	s_cmp_eq_u32 s20, 0x660000
	s_waitcnt vmcnt(2)
	ds_write_b128 v82, v[178:181] offset:32768
	v_mfma_f32_32x32x16_bf16 v[50:65], v[90:93], v[106:109], v[50:65]
	s_waitcnt vmcnt(1)
	ds_write_b128 v83, v[170:173]
	s_waitcnt vmcnt(0)
	ds_write_b128 v83, v[174:177] offset:8192
	s_waitcnt lgkmcnt(0)
	s_barrier
	v_mfma_f32_32x32x16_bf16 v[50:65], v[94:97], v[240:243], v[50:65]
	s_cbranch_scc0 .LBB0_1200
	ds_read_b128 v[98:101], v217 offset:57344
	ds_read_b128 v[102:105], v218 offset:12288
	s_waitcnt lgkmcnt(1)
	v_mfma_f32_32x32x16_bf16 v[82:97], v[98:101], v[158:161], v[66:81]
	ds_read_b128 v[98:101], v219 offset:57344
	s_waitcnt lgkmcnt(1)
	v_mfma_f32_32x32x16_bf16 v[66:81], v[102:105], v[158:161], v[66:81]
	s_waitcnt lgkmcnt(0)
	v_mfma_f32_32x32x16_bf16 v[82:97], v[98:101], v[154:157], v[82:97]
	ds_read_b128 v[98:101], v220 offset:12288
	s_waitcnt lgkmcnt(0)
	v_mfma_f32_32x32x16_bf16 v[66:81], v[98:101], v[154:157], v[66:81]
	ds_read_b128 v[98:101], v221 offset:57344
	s_waitcnt lgkmcnt(0)
	v_mfma_f32_32x32x16_bf16 v[82:97], v[98:101], v[150:153], v[82:97]
	ds_read_b128 v[98:101], v222 offset:12288
	s_waitcnt lgkmcnt(0)
	v_mfma_f32_32x32x16_bf16 v[66:81], v[98:101], v[150:153], v[66:81]
	ds_read_b128 v[98:101], v223 offset:57344
	s_waitcnt lgkmcnt(0)
	v_mfma_f32_32x32x16_bf16 v[82:97], v[98:101], v[146:149], v[82:97]
	ds_read_b128 v[98:101], v224 offset:12288
	s_waitcnt lgkmcnt(0)
	v_mfma_f32_32x32x16_bf16 v[66:81], v[98:101], v[146:149], v[66:81]
	ds_read_b128 v[98:101], v217 offset:57472
	ds_read_b128 v[102:105], v218 offset:12416
	s_waitcnt lgkmcnt(1)
	v_mfma_f32_32x32x16_bf16 v[82:97], v[98:101], v[142:145], v[82:97]
	ds_read_b128 v[98:101], v219 offset:57472
	s_waitcnt lgkmcnt(1)
	v_mfma_f32_32x32x16_bf16 v[66:81], v[102:105], v[142:145], v[66:81]
	s_waitcnt lgkmcnt(0)
	v_mfma_f32_32x32x16_bf16 v[82:97], v[98:101], v[138:141], v[82:97]
	ds_read_b128 v[98:101], v220 offset:12416
	s_waitcnt lgkmcnt(0)
	v_mfma_f32_32x32x16_bf16 v[66:81], v[98:101], v[138:141], v[66:81]
	ds_read_b128 v[98:101], v221 offset:57472
	s_waitcnt lgkmcnt(0)
	v_mfma_f32_32x32x16_bf16 v[82:97], v[98:101], v[134:137], v[82:97]
	ds_read_b128 v[98:101], v222 offset:12416
	s_waitcnt lgkmcnt(0)
	v_mfma_f32_32x32x16_bf16 v[66:81], v[98:101], v[134:137], v[66:81]
	ds_read_b128 v[98:101], v223 offset:57472
	s_waitcnt lgkmcnt(0)
	v_mfma_f32_32x32x16_bf16 v[82:97], v[98:101], v[130:133], v[82:97]
	ds_read_b128 v[98:101], v224 offset:12416
	s_waitcnt lgkmcnt(0)
	v_mfma_f32_32x32x16_bf16 v[66:81], v[98:101], v[130:133], v[66:81]
	ds_read_b128 v[98:101], v217 offset:57600
	ds_read_b128 v[102:105], v218 offset:12544
	s_waitcnt lgkmcnt(1)
	v_mfma_f32_32x32x16_bf16 v[82:97], v[98:101], v[126:129], v[82:97]
	ds_read_b128 v[98:101], v219 offset:57600
	s_waitcnt lgkmcnt(1)
	v_mfma_f32_32x32x16_bf16 v[66:81], v[102:105], v[126:129], v[66:81]
	s_waitcnt lgkmcnt(0)
; #define PSUB_AT(k) do { if (PROBE_SUB == (k) && DK == PROBE_SUBDK) sacc = __builtin_amdgcn_readfirstlane(sacc + ((unsigned)__builtin_readcyclecounter() - ps_t0_)); } while (0)
; #define SBAR() __builtin_amdgcn_sched_barrier(0)
; #define SLOAD(k0) do { const unsigned so_k = (unsigned)((k0) * ldk) * 2u, so_v = (unsigned)((k0) * ldv) * 2u; \
;         _Pragma("unroll") for (int i = 0; i < KP; ++i) ks[i] = __builtin_amdgcn_raw_buffer_load_b128(krs, kgo[i], so_k, 0); \
;         vs0 = __builtin_amdgcn_raw_buffer_load_b128(vrs, vgo, so_v, 0); vs1 = __builtin_amdgcn_raw_buffer_load_b128(vrs, vgo + vstep, so_v, 0); } while (0)
; template <int DK, bool PF, bool EARLY, bool PFD = false> ...
;     ...
;         const char* Kb = K_lds + cur * SHM_K;
; #pragma unroll
;         for (int d0 = 0; d0 < NQ; ++d0) {
;             const bf16x8 b0 = *reinterpret_cast<const bf16x8*>(Kb + kra_(d0 & 3) + (d0 >> 2) * 128);
;             const bf16x8 b1 = *reinterpret_cast<const bf16x8*>(Kb + kra_(d0 & 3) + (d0 >> 2) * 128 + 32 * DK * 2);
;             p0 = __builtin_amdgcn_mfma_f32_32x32x16_bf16(b0, qr[d0], p0, 0, 0, 0);
;             p1 = __builtin_amdgcn_mfma_f32_32x32x16_bf16(b1, qr[d0], p1, 0, 0, 0);
;             if ((d0 & 3) == 3) SBAR();
;         }
;         PSUB_AT(1);
;         if (!EARLY && j + 1 < ntile) SLOAD((j + 1) * 64);
;         float ps = 0.f, ps1 = 0.f;
; #pragma unroll
;         for (int r = 0; r < 16; ++r) { p0[r] = __builtin_amdgcn_exp2f(p0[r]); p1[r] = __builtin_amdgcn_exp2f(p1[r]); ps += p0[r]; asm("" : "+v"(ps)); ps1 += p1[r]; asm("" : "+v"(ps1)); }
;         l_reg += ps + ps1;
;         bf16x8 pa0, pa1, pa2, pa3;
;     ...
;         PK4(p0, 0, pa0); PK4(p0, 8, pa1); PK4(p1, 0, pa2); PK4(p1, 8, pa3);
;     ...
;         PSUB_AT(2);
;         const int vb = vb0 + cur * SHM_V;
;         pv_one<0>(o[0], vb, pa0, pa1, pa2, pa3); pv_one<1>(o[1], vb, pa0, pa1, pa2, pa3); pv_one<2>(o[2], vb, pa0, pa1, pa2, pa3); pv_one<3>(o[3], vb, pa0, pa1, pa2, pa3);
; __device__ __forceinline__ void row_recip(float l_reg, float* li_l  , int r32, int hi, float (&rli)[16]) {
;     { auto rr = __builtin_amdgcn_permlane32_swap(__float_as_uint(l_reg), __float_as_uint(l_reg), false, false); l_reg = __uint_as_float(rr[0]) + __uint_as_float(rr[1]); }
;     if (hi == 0) li_l[r32] = l_reg;
	v_mfma_f32_32x32x16_bf16 v[82:97], v[98:101], v[122:125], v[82:97]
	ds_read_b128 v[98:101], v220 offset:12544
	s_waitcnt lgkmcnt(0)
	v_mfma_f32_32x32x16_bf16 v[66:81], v[98:101], v[122:125], v[66:81]
	ds_read_b128 v[98:101], v221 offset:57600
	s_waitcnt lgkmcnt(0)
	v_mfma_f32_32x32x16_bf16 v[82:97], v[98:101], v[118:121], v[82:97]
	ds_read_b128 v[98:101], v222 offset:12544
	s_waitcnt lgkmcnt(0)
	v_mfma_f32_32x32x16_bf16 v[66:81], v[98:101], v[118:121], v[66:81]
	ds_read_b128 v[98:101], v223 offset:57600
	s_waitcnt lgkmcnt(0)
	v_mfma_f32_32x32x16_bf16 v[82:97], v[98:101], v[114:117], v[82:97]
	ds_read_b128 v[98:101], v224 offset:12544
	s_waitcnt lgkmcnt(0)
	v_mfma_f32_32x32x16_bf16 v[66:81], v[98:101], v[114:117], v[66:81]
	s_nop 11
	v_exp_f32_e32 v98, v66
	v_exp_f32_e32 v82, v82
	v_exp_f32_e32 v67, v67
	v_exp_f32_e32 v83, v83
	v_add_f32_e32 v99, 0, v98
	v_exp_f32_e32 v100, v68
	v_add_f32_e32 v66, 0, v82
	v_exp_f32_e32 v84, v84
	v_add_f32_e32 v99, v67, v99
	v_exp_f32_e32 v85, v85
	v_add_f32_e32 v66, v83, v66
	v_add_f32_e32 v68, v100, v99
	v_exp_f32_e32 v99, v69
	v_exp_f32_e32 v86, v86
	v_add_f32_e32 v66, v84, v66
	v_exp_f32_e32 v101, v70
	v_exp_f32_e32 v70, v87
	v_add_f32_e32 v66, v85, v66
	v_add_f32_e32 v68, v99, v68
	v_exp_f32_e32 v87, v71
	v_exp_f32_e32 v71, v88
	v_add_f32_e32 v66, v86, v66
	v_add_f32_e32 v68, v101, v68
	v_exp_f32_e32 v88, v72
	v_exp_f32_e32 v72, v89
	v_add_f32_e32 v66, v70, v66
	v_add_f32_e32 v68, v87, v68
	v_exp_f32_e32 v89, v73
	v_exp_f32_e32 v73, v90
	v_add_f32_e32 v66, v71, v66
	v_add_f32_e32 v68, v88, v68
	v_exp_f32_e32 v90, v74
	v_exp_f32_e32 v74, v91
	v_add_f32_e32 v66, v72, v66
	v_add_f32_e32 v68, v89, v68
	v_exp_f32_e32 v91, v75
	v_exp_f32_e32 v75, v92
	v_add_f32_e32 v66, v73, v66
	v_add_f32_e32 v68, v90, v68
	v_exp_f32_e32 v92, v76
	v_exp_f32_e32 v76, v93
	v_add_f32_e32 v66, v74, v66
	v_add_f32_e32 v68, v91, v68
	v_exp_f32_e32 v93, v77
	v_exp_f32_e32 v77, v94
	v_add_f32_e32 v66, v75, v66
	v_add_f32_e32 v68, v92, v68
	v_exp_f32_e32 v94, v78
	v_exp_f32_e32 v78, v95
	v_add_f32_e32 v66, v76, v66
	v_add_f32_e32 v68, v93, v68
	v_exp_f32_e32 v95, v79
	v_exp_f32_e32 v79, v96
	v_add_f32_e32 v66, v77, v66
	v_add_f32_e32 v68, v94, v68
	v_exp_f32_e32 v96, v80
	v_exp_f32_e32 v80, v97
	v_add_f32_e32 v66, v78, v66
	v_add_f32_e32 v68, v95, v68
	v_exp_f32_e32 v97, v81
	s_nop 0
	v_add_f32_e32 v66, v79, v66
	v_add_f32_e32 v68, v96, v68
	s_nop 0
	v_add_f32_e32 v66, v80, v66
	v_add_f32_e32 v68, v97, v68
	s_nop 0
	v_add_f32_e32 v66, v66, v68
	v_cvt_pk_bf16_f32 v68, v82, v83
	v_cvt_pk_bf16_f32 v69, v84, v85
	v_cvt_pk_bf16_f32 v70, v86, v70
	v_cvt_pk_bf16_f32 v71, v71, v72
	v_cvt_pk_bf16_f32 v72, v73, v74
	v_cvt_pk_bf16_f32 v73, v75, v76
	v_cvt_pk_bf16_f32 v74, v77, v78
	v_cvt_pk_bf16_f32 v75, v79, v80
	v_cvt_pk_bf16_f32 v76, v98, v67
	v_cvt_pk_bf16_f32 v77, v100, v99
	v_cvt_pk_bf16_f32 v78, v101, v87
	v_cvt_pk_bf16_f32 v79, v88, v89
	v_cvt_pk_bf16_f32 v80, v90, v91
	v_cvt_pk_bf16_f32 v81, v92, v93
	v_cvt_pk_bf16_f32 v82, v94, v95
	v_cvt_pk_bf16_f32 v83, v96, v97
	ds_read_b64_tr_b16 v[84:85], v225 offset:0
	ds_read_b64_tr_b16 v[86:87], v225 offset:0x800
	ds_read_b64_tr_b16 v[88:89], v225 offset:0x1000
	ds_read_b64_tr_b16 v[90:91], v225 offset:0x1800
	ds_read_b64_tr_b16 v[92:93], v225 offset:0x2000
	ds_read_b64_tr_b16 v[94:95], v225 offset:0x2800
	ds_read_b64_tr_b16 v[96:97], v225 offset:0x3000
	ds_read_b64_tr_b16 v[98:99], v225 offset:0x3800
	s_waitcnt lgkmcnt(0)
	v_add_f32_e32 v66, v188, v66
	v_mfma_f32_32x32x16_bf16 v[2:17], v[68:71], v[84:87], v[2:17]
	ds_read_b64_tr_b16 v[84:85], v225 offset:0x200
	ds_read_b64_tr_b16 v[86:87], v225 offset:0xa00
	v_mfma_f32_32x32x16_bf16 v[2:17], v[72:75], v[88:91], v[2:17]
	ds_read_b64_tr_b16 v[88:89], v225 offset:0x1200
	ds_read_b64_tr_b16 v[90:91], v225 offset:0x1a00
	v_mfma_f32_32x32x16_bf16 v[2:17], v[76:79], v[92:95], v[2:17]
	ds_read_b64_tr_b16 v[92:93], v225 offset:0x2200
	ds_read_b64_tr_b16 v[94:95], v225 offset:0x2a00
	ds_read_b64_tr_b16 v[100:101], v225 offset:0x3200
	ds_read_b64_tr_b16 v[102:103], v225 offset:0x3a00
	s_waitcnt lgkmcnt(0)
	v_mfma_f32_32x32x16_bf16 v[2:17], v[80:83], v[96:99], v[2:17]
	v_mfma_f32_32x32x16_bf16 v[18:33], v[68:71], v[84:87], v[18:33]
	ds_read_b64_tr_b16 v[84:85], v225 offset:0x400
	ds_read_b64_tr_b16 v[86:87], v225 offset:0xc00
	v_mfma_f32_32x32x16_bf16 v[18:33], v[72:75], v[88:91], v[18:33]
	ds_read_b64_tr_b16 v[88:89], v225 offset:0x1400
	ds_read_b64_tr_b16 v[90:91], v225 offset:0x1c00
	v_mfma_f32_32x32x16_bf16 v[18:33], v[76:79], v[92:95], v[18:33]
	ds_read_b64_tr_b16 v[92:93], v225 offset:0x2400
	ds_read_b64_tr_b16 v[94:95], v225 offset:0x2c00
	ds_read_b64_tr_b16 v[96:97], v225 offset:0x3400
	ds_read_b64_tr_b16 v[98:99], v225 offset:0x3c00
	s_waitcnt lgkmcnt(0)
	v_mfma_f32_32x32x16_bf16 v[18:33], v[80:83], v[100:103], v[18:33]
	v_mfma_f32_32x32x16_bf16 v[34:49], v[68:71], v[84:87], v[34:49]
	ds_read_b64_tr_b16 v[84:85], v225 offset:0x600
	ds_read_b64_tr_b16 v[86:87], v225 offset:0xe00
	v_mfma_f32_32x32x16_bf16 v[34:49], v[72:75], v[88:91], v[34:49]
	ds_read_b64_tr_b16 v[88:89], v225 offset:0x1600
	ds_read_b64_tr_b16 v[90:91], v225 offset:0x1e00
	v_mfma_f32_32x32x16_bf16 v[34:49], v[76:79], v[92:95], v[34:49]
	ds_read_b64_tr_b16 v[92:93], v225 offset:0x2600
	ds_read_b64_tr_b16 v[94:95], v225 offset:0x2e00
	ds_read_b64_tr_b16 v[100:101], v225 offset:0x3600
	ds_read_b64_tr_b16 v[102:103], v225 offset:0x3e00
	s_waitcnt lgkmcnt(0)
	v_mfma_f32_32x32x16_bf16 v[34:49], v[80:83], v[96:99], v[34:49]
	v_mfma_f32_32x32x16_bf16 v[50:65], v[68:71], v[84:87], v[50:65]
	s_barrier
	v_mfma_f32_32x32x16_bf16 v[50:65], v[72:75], v[88:91], v[50:65]
	v_mfma_f32_32x32x16_bf16 v[50:65], v[76:79], v[92:95], v[50:65]
	v_mfma_f32_32x32x16_bf16 v[50:65], v[80:83], v[100:103], v[50:65]
	s_setprio 0
	v_mov_b32_e32 v67, v66
	s_nop 1
	v_permlane32_swap_b32_e32 v66, v67
	s_and_saveexec_b64 s[8:9], s[6:7]
	s_cbranch_execz .LBB0_1186
	v_add_f32_e32 v66, v66, v67
	ds_write_b32 v227, v66
	s_branch .LBB0_1186

; __device__ __forceinline__ int v_st(int k, int c) { const int kk = (k & ~0xC) | ((k & 4) << 1) | ((k & 8) >> 1); return ((kk >> 3) * 4 + (c >> 5)) * 512 + ((kk & 7) * 32 + (c & 31)) * 2; }
; __device__ __forceinline__ int v_rd_base(int lane) { return ((lane & 3) << 3) | (((lane >> 2) & 3) << 6) | (((lane >> 4) & 1) << 5) | (((lane >> 5) & 1) << 8); }
; #define SLOAD(k0) do { const unsigned so_k = (unsigned)((k0) * ldk) * 2u, so_v = (unsigned)((k0) * ldv) * 2u; \
;         _Pragma("unroll") for (int i = 0; i < KP; ++i) ks[i] = __builtin_amdgcn_raw_buffer_load_b128(krs, kgo[i], so_k, 0); \
;         vs0 = __builtin_amdgcn_raw_buffer_load_b128(vrs, vgo, so_v, 0); vs1 = __builtin_amdgcn_raw_buffer_load_b128(vrs, vgo + vstep, so_v, 0); } while (0)
; template <int DK, bool PF, bool EARLY, bool PFD = false> ...
;     ...
;     const int tid = threadIdx.x, lane = tid & 63, r32 = lane & 31, hi = lane >> 5;
;     char* V_lds = lds_kv; char* K_lds = lds_kv + 2 * SHM_V;
;     bf16x8 qr[NQ];
; #pragma unroll
;     for (int d0 = 0; d0 < NQ; ++d0) qr[d0] = *reinterpret_cast<const bf16x8*>(Qrow + d0 * 16);
;     const __amdgpu_buffer_rsrc_t krs = __builtin_amdgcn_make_buffer_rsrc((void*)Kh, 0, nkeys * ldk * 2, 0x00020000);
;     const __amdgpu_buffer_rsrc_t vrs = __builtin_amdgcn_make_buffer_rsrc((void*)Vh, 0, nkeys * ldv * 2, 0x00020000);
;     unsigned kgo[KP]; int kst[KP];
; #pragma unroll
;     for (int i = 0; i < KP; ++i) { const int p = tid + i * NT, row = p / CH, ch = p % CH; kgo[i] = (unsigned)(row * ldk + ch * 8) * 2u; kst[i] = kswz<DK>(row, ch); }
;     const int vrow0 = tid >> 4, vc = (tid & 15) * 8;
;     const unsigned vgo = (unsigned)(vrow0 * ldv + vc) * 2u, vstep = (unsigned)(32 * ldv) * 2u;
;     const int vst0 = v_st(vrow0, vc); constexpr int vst1d = 8192;
;     const int vb0 = (int)(uintptr_t)V_lds + v_rd_base(lane);
;     const int kbase = r32 * (DK * 2), kt0 = (hi ^ ((r32 >> 1) & 7)) << 4;
;     ...
;     u32x4 ks[KP], vs0, vs1;
;     ...
;     constexpr int KLINES = (64 * DK * 2) / 128, VLINES = 128, LPR = DK / 64;
;     unsigned pf_dummy = 0u;
;     ...
;     const int ntile = nkeys / 64;
;     if (tid >= 256) __builtin_amdgcn_s_setprio(1);
;     PREFETCH(1); PREFETCH(2);
;     SLOAD(0); SWRITE(0); __syncthreads();
.LBB0_1915:
	s_cmp_lt_i32 s96, 14
	s_cselect_b64 s[0:1], -1, 0
	s_cmp_gt_i32 s97, 13
	s_cselect_b64 s[4:5], -1, 0
	s_and_b64 s[0:1], s[0:1], s[4:5]
	v_readlane_b32 s3, v254, 2
	s_cmpk_lt_i32 s3, 0x200
	s_cselect_b64 s[4:5], -1, 0
	s_and_b64 s[4:5], s[0:1], s[4:5]
	s_andn2_b64 vcc, exec, s[4:5]
	s_waitcnt vmcnt(0)
	v_lshlrev_b32_e32 v188, 3, v0
	s_cbranch_vccnz .LBB0_2067
	v_lshlrev_b32_e32 v2, 2, v0
	v_lshrrev_b32_e32 v14, 4, v0
	v_and_b32_e32 v3, 0x700, v2
	v_lshlrev_b32_e32 v2, 9, v0
	s_mov_b32 s4, 0x7f800
	v_mov_b32_e32 v4, 0x40000
	v_lshrrev_b32_e32 v10, 3, v0
	v_mul_u32_u24_e32 v15, 0xc00, v14
	v_and_b32_e32 v14, 16, v14
	v_bitop3_b32 v152, v2, s4, v4 bitop3:0xc8
	v_mul_u32_u24_e32 v4, 0x1800, v10
	v_lshlrev_b32_e32 v12, 7, v10
	v_and_or_b32 v10, v10, 8, v14
	s_ashr_i32 s3, s62, 31
	s_waitcnt lgkmcnt(0)
	s_ashr_i32 s38, s2, 31
	v_lshrrev_b32_e32 v8, 5, v0
	v_lshrrev_b32_e32 v10, 1, v10
	v_bfe_u32 v14, v188, 5, 2
	v_bfe_u32 v17, v0, 1, 3
	s_add_u32 s39, s78, 0x3e53e000
	v_or_b32_e32 v10, v10, v14
	v_and_or_b32 v14, v8, 4, v185
	v_bitop3_b32 v8, v8, v17, 1 bitop3:0x6c
	s_addc_u32 s40, s79, 0
	v_lshlrev_b32_e32 v187, 4, v8
	v_subrev_co_u32_e64 v8, s[8:9], 64, v0
	v_and_b32_e32 v150, 0x3f800, v2
	v_mov_b32_e32 v2, 0x100
	s_add_u32 s24, s78, 0x13c004
	s_movk_i32 s42, 0xc00
	v_lshrrev_b32_e32 v189, 1, v8
	v_lshlrev_b32_e32 v8, 6, v8
	v_lshl_or_b32 v154, v1, 5, v2
	s_addc_u32 s25, s79, 0
	v_and_b32_e32 v2, 0x1c0, v0
	s_add_i32 s4, 0, 0x1f800
	v_mul_lo_u32 v17, v189, s42
	v_and_b32_e32 v190, 64, v8
	v_lshlrev_b32_e32 v5, 7, v0
	v_lshl_add_u32 v9, v2, 2, s4
	v_lshlrev_b32_e32 v11, 4, v0
	s_movk_i32 s4, 0x70
	v_or_b32_e32 v8, v17, v190
	v_and_b32_e32 v146, 0x180, v5
	v_and_or_b32 v145, v11, s4, v4
	v_and_b32_e32 v4, 0x78, v188
	v_and_b32_e32 v5, 0xf80, v5
	s_xor_b64 s[26:27], s[8:9], -1
	v_lshlrev_b32_e32 v8, 1, v8
	s_add_i32 s10, 0, 0x18000
	s_add_i32 s11, 0, 0x10000
	s_movk_i32 s41, 0x1800
	v_bitop3_b32 v13, v11, s4, v0 bitop3:0x48
	v_or_b32_e32 v15, v15, v4
	v_lshlrev_b32_e32 v16, 1, v0
	v_add_u32_e32 v191, 0x60000, v8
	v_add_u32_e32 v193, 0xc0000, v8
	v_mov_b32_e32 v8, 0xc0000
	v_add_u32_e32 v198, s10, v5
	v_and_b32_e32 v5, 0x118, v188
	s_cmp_lg_u32 s11, -1
	v_bfe_u32 v6, v0, 5, 1
	v_lshlrev_b32_e32 v186, 1, v15
	v_lshlrev_b32_e32 v14, 6, v14
	v_and_b32_e32 v15, 48, v11
	v_and_b32_e32 v11, 0xc0, v11
	v_mad_u32_u24 v194, v0, s41, v8
	v_add3_u32 v196, s10, v13, v12
	v_lshl_add_u32 v8, v10, 9, s11
	v_and_or_b32 v5, v16, 32, v5
	s_cselect_b32 s10, s11, 0
	v_lshl_add_u32 v7, v1, 13, 0
	v_lshlrev_b32_e32 v2, 3, v6
	v_add3_u32 v197, v8, v14, v15
	v_lshrrev_b32_e32 v226, 3, v197
	v_xor_b32_e32 v226, v226, v197
	v_and_b32_e32 v226, 0x100, v226
	v_xor_b32_e32 v197, v197, v226
	v_lshlrev_b32_e32 v226, 3, v226
	v_xor_b32_e32 v197, v197, v226
	v_add3_u32 v199, v11, s10, v5
	v_lshlrev_b32_e32 v5, 4, v6
	v_lshlrev_b32_e32 v8, 1, v184
	v_lshlrev_b32_e32 v6, 10, v6
	v_mov_b32_e32 v17, 0x60000
	v_add3_u32 v205, v7, v8, v6
	v_readlane_b32 s80, v254, 3
	v_or_b32_e32 v8, 4, v185
	v_or_b32_e32 v10, 8, v185
	v_or_b32_e32 v12, 12, v185
	v_or_b32_e32 v14, 16, v185
	v_or_b32_e32 v16, 20, v185
	v_or_b32_e32 v18, 24, v185
	v_or_b32_e32 v20, 28, v185
	v_mov_b32_e32 v149, 0
	s_movk_i32 s6, 0xc0
	s_movk_i32 s4, 0xff
	v_mad_u32_u24 v192, v0, s41, v17
	v_lshl_add_u32 v7, v4, 1, v7
	v_lshlrev_b32_e32 v148, 2, v4
	v_readlane_b32 s94, v254, 17
	v_readlane_b32 s95, v254, 18
	v_lshlrev_b32_e32 v11, 8, v185
	v_lshlrev_b32_e32 v6, 10, v185
	v_lshlrev_b32_e32 v13, 8, v8
	v_lshlrev_b32_e32 v8, 10, v8
	v_lshlrev_b32_e32 v15, 8, v10
	v_lshlrev_b32_e32 v10, 10, v10
	v_lshlrev_b32_e32 v17, 8, v12
	v_lshlrev_b32_e32 v12, 10, v12
	v_lshlrev_b32_e32 v19, 8, v14
	v_lshlrev_b32_e32 v14, 10, v14
	v_lshlrev_b32_e32 v21, 8, v16
	v_lshlrev_b32_e32 v16, 10, v16
	v_lshlrev_b32_e32 v22, 8, v18
	v_lshlrev_b32_e32 v18, 10, v18
	v_lshlrev_b32_e32 v23, 8, v20
	v_lshlrev_b32_e32 v20, 10, v20
	s_add_i32 s12, 0, 0x23140
	s_mov_b32 s14, 0x1980000
	s_mov_b32 s15, 0x20000
	v_mov_b32_e32 v147, v149
	v_mov_b32_e32 v151, v149
	v_mov_b32_e32 v153, v149
	v_mov_b32_e32 v155, v149
	v_cmp_lt_u32_e64 s[4:5], s4, v0
	v_cmp_gt_u32_e64 s[6:7], s6, v0
	v_add_u32_e32 v195, 0x30000, v186
	v_xor_b32_e32 v200, 32, v187
	v_xor_b32_e32 v201, 64, v187
	v_xor_b32_e32 v202, 0x60, v187
	v_add_u32_e32 v203, 0x4000, v199
	v_cmp_gt_u32_e64 s[10:11], 32, v182
	v_lshl_add_u32 v204, v184, 2, v9
	v_lshl_add_u64 v[156:157], s[94:95], 0, v[148:149]
	v_mul_u32_u24_e32 v206, 0x1800, v0
	v_add_u32_e32 v207, s12, v3
	v_lshlrev_b32_e32 v148, 1, v2
	s_mov_b32 s18, s14
	s_mov_b32 s19, s15
	v_add_u32_e32 v208, v9, v5
	s_movk_i32 s43, 0x7fff
	v_lshlrev_b32_e32 v158, 1, v4
	v_add_u32_e32 v209, v7, v11
	v_mov_b32_e32 v210, 0x358637bd
	s_mov_b32 s44, 0x800000
	v_lshlrev_b32_e32 v160, 1, v6
	v_add_u32_e32 v211, v7, v13
	v_lshlrev_b32_e32 v162, 1, v8
	v_add_u32_e32 v212, v7, v15
	v_lshlrev_b32_e32 v164, 1, v10
	v_add_u32_e32 v213, v7, v17
	v_lshlrev_b32_e32 v166, 1, v12
	v_add_u32_e32 v214, v7, v19
	v_lshlrev_b32_e32 v168, 1, v14
	v_add_u32_e32 v215, v7, v21
	v_lshlrev_b32_e32 v170, 1, v16
	v_add_u32_e32 v216, v7, v22
	v_lshlrev_b32_e32 v172, 1, v18
	v_add_u32_e32 v217, v7, v23
	v_lshlrev_b32_e32 v174, 1, v20
	v_mov_b64_e32 v[176:177], 0xff
	v_readlane_b32 s22, v254, 2
	v_readlane_b32 s81, v254, 4
	v_readlane_b32 s82, v254, 5
	v_readlane_b32 s83, v254, 6
	v_readlane_b32 s84, v254, 7
	v_readlane_b32 s85, v254, 8
	v_readlane_b32 s86, v254, 9
	v_readlane_b32 s87, v254, 10
	v_readlane_b32 s88, v254, 11
	v_readlane_b32 s89, v254, 12
	v_readlane_b32 s90, v254, 13
	v_readlane_b32 s91, v254, 14
	v_readlane_b32 s92, v254, 15
	v_readlane_b32 s93, v254, 16
	s_branch .LBB0_1918

; #define PSUB_AT(k) do { if (PROBE_SUB == (k) && DK == PROBE_SUBDK) sacc = __builtin_amdgcn_readfirstlane(sacc + ((unsigned)__builtin_readcyclecounter() - ps_t0_)); } while (0)
; #define SBAR() __builtin_amdgcn_sched_barrier(0)
; #define SLOAD(k0) do { const unsigned so_k = (unsigned)((k0) * ldk) * 2u, so_v = (unsigned)((k0) * ldv) * 2u; \
;         _Pragma("unroll") for (int i = 0; i < KP; ++i) ks[i] = __builtin_amdgcn_raw_buffer_load_b128(krs, kgo[i], so_k, 0); \
;         vs0 = __builtin_amdgcn_raw_buffer_load_b128(vrs, vgo, so_v, 0); vs1 = __builtin_amdgcn_raw_buffer_load_b128(vrs, vgo + vstep, so_v, 0); } while (0)
; template <int DK, bool PF, bool EARLY, bool PFD = false> ...
;     ...
;         if (EARLY && j + 1 < ntile) SLOAD((j + 1) * 64);
;         f32x16 p0, p1;
; #pragma unroll
;         for (int r = 0; r < 16; ++r) { p0[r] = negM; p1[r] = negM; }
;         const char* Kb = K_lds + cur * SHM_K;
; #pragma unroll
;         for (int d0 = 0; d0 < NQ; ++d0) {
;             const bf16x8 b0 = *reinterpret_cast<const bf16x8*>(Kb + kra_(d0 & 3) + (d0 >> 2) * 128);
;             const bf16x8 b1 = *reinterpret_cast<const bf16x8*>(Kb + kra_(d0 & 3) + (d0 >> 2) * 128 + 32 * DK * 2);
;             p0 = __builtin_amdgcn_mfma_f32_32x32x16_bf16(b0, qr[d0], p0, 0, 0, 0);
;             p1 = __builtin_amdgcn_mfma_f32_32x32x16_bf16(b1, qr[d0], p1, 0, 0, 0);
;             if ((d0 & 3) == 3) SBAR();
;         }
;         PSUB_AT(1);
;         if (!EARLY && j + 1 < ntile) SLOAD((j + 1) * 64);
;         float ps = 0.f, ps1 = 0.f;
; #pragma unroll
;         for (int r = 0; r < 16; ++r) { p0[r] = __builtin_amdgcn_exp2f(p0[r]); p1[r] = __builtin_amdgcn_exp2f(p1[r]); ps += p0[r]; asm("" : "+v"(ps)); ps1 += p1[r]; asm("" : "+v"(ps1)); }
;         l_reg += ps + ps1;
;         bf16x8 pa0, pa1, pa2, pa3;
;     ...
;         PK4(p0, 0, pa0); PK4(p0, 8, pa1); PK4(p1, 0, pa2); PK4(p1, 8, pa3);
;     ...
;         PSUB_AT(2);
;         const int vb = vb0 + cur * SHM_V;
;         pv_one<0>(o[0], vb, pa0, pa1, pa2, pa3); pv_one<1>(o[1], vb, pa0, pa1, pa2, pa3); pv_one<2>(o[2], vb, pa0, pa1, pa2, pa3); pv_one<3>(o[3], vb, pa0, pa1, pa2, pa3);
.LBB0_1932:
	s_and_b32 s13, s50, 1
	s_lshl_b32 s12, s13, 13
	v_add_u32_e32 v138, s12, v198
	v_add_u32_e32 v86, v138, v187
	v_add_u32_e32 v134, v138, v200
	v_add_u32_e32 v135, v138, v201
	v_add_u32_e32 v136, v138, v202
	ds_read_b128 v[226:229], v86
	ds_read_b128 v[230:233], v86 offset:4096
	ds_read_b128 v[234:237], v134
	ds_read_b128 v[238:241], v134 offset:4096
	ds_read_b128 v[242:245], v135
	ds_read_b128 v[246:249], v135 offset:4096
	ds_read_b128 v[250:253], v136
	ds_read_b128 v[218:221], v136 offset:4096
	s_add_i32 s33, s51, 0xfff40000
	buffer_load_dwordx4 v[130:133], v145, s[16:19], s33 offen
	buffer_load_dwordx4 v[134:137], v186, s[20:23], s33 offen
	buffer_load_dwordx4 v[138:141], v195, s[20:23], s33 offen
	s_waitcnt lgkmcnt(7)
	v_mfma_f32_32x32x16_bf16 v[98:113], v[226:229], v[126:129], v[2:17]
	s_waitcnt lgkmcnt(6)
	v_mfma_f32_32x32x16_bf16 v[82:97], v[230:233], v[126:129], v[2:17]
	s_waitcnt lgkmcnt(5)
	v_mfma_f32_32x32x16_bf16 v[98:113], v[234:237], v[122:125], v[98:113]
	s_waitcnt lgkmcnt(4)
	v_mfma_f32_32x32x16_bf16 v[82:97], v[238:241], v[122:125], v[82:97]
	s_waitcnt lgkmcnt(3)
	v_mfma_f32_32x32x16_bf16 v[98:113], v[242:245], v[118:121], v[98:113]
	s_waitcnt lgkmcnt(2)
	v_mfma_f32_32x32x16_bf16 v[82:97], v[246:249], v[118:121], v[82:97]
	s_waitcnt lgkmcnt(1)
	v_mfma_f32_32x32x16_bf16 v[98:113], v[250:253], v[114:117], v[98:113]
	s_waitcnt lgkmcnt(0)
	v_mfma_f32_32x32x16_bf16 v[82:97], v[218:221], v[114:117], v[82:97]
	s_lshl_b32 s13, s13, 14
	v_add_u32_e32 v253, s13, v199
	ds_read_b64_tr_b16 v[226:227], v253 offset:0x0
	ds_read_b64_tr_b16 v[228:229], v253 offset:0x800
	ds_read_b64_tr_b16 v[230:231], v253 offset:0x1000
	ds_read_b64_tr_b16 v[232:233], v253 offset:0x1800
	ds_read_b64_tr_b16 v[234:235], v253 offset:0x2000
	ds_read_b64_tr_b16 v[236:237], v253 offset:0x2800
	ds_read_b64_tr_b16 v[238:239], v253 offset:0x3000
	ds_read_b64_tr_b16 v[240:241], v253 offset:0x3800
	s_nop 0
	v_exp_f32_e32 v98, v98
	s_nop 1
	v_exp_f32_e32 v159, v82
	v_exp_f32_e32 v99, v99
	v_exp_f32_e32 v163, v83
	v_add_f32_e32 v82, 0, v98
	v_add_f32_e32 v161, 0, v159
	v_exp_f32_e32 v100, v100
	v_exp_f32_e32 v101, v101
	v_add_f32_e32 v82, v99, v82
	v_add_f32_e32 v83, v163, v161
	v_exp_f32_e32 v161, v84
	v_exp_f32_e32 v165, v85
	v_add_f32_e32 v82, v100, v82
	v_exp_f32_e32 v102, v102
	v_exp_f32_e32 v167, v86
	v_add_f32_e32 v83, v161, v83
	v_add_f32_e32 v82, v101, v82
	v_exp_f32_e32 v86, v103
	v_exp_f32_e32 v103, v87
	v_add_f32_e32 v83, v165, v83
	v_add_f32_e32 v82, v102, v82
	v_exp_f32_e32 v87, v104
	v_exp_f32_e32 v104, v88
	v_add_f32_e32 v83, v167, v83
	v_add_f32_e32 v82, v86, v82
	v_exp_f32_e32 v88, v105
	v_exp_f32_e32 v105, v89
	v_add_f32_e32 v83, v103, v83
	v_add_f32_e32 v82, v87, v82
	v_exp_f32_e32 v89, v106
	v_exp_f32_e32 v106, v90
	v_add_f32_e32 v83, v104, v83
	v_add_f32_e32 v82, v88, v82
	v_exp_f32_e32 v90, v107
	v_exp_f32_e32 v107, v91
	v_add_f32_e32 v83, v105, v83
	v_add_f32_e32 v82, v89, v82
	v_exp_f32_e32 v91, v108
	v_exp_f32_e32 v108, v92
	v_add_f32_e32 v83, v106, v83
	v_add_f32_e32 v82, v90, v82
	v_exp_f32_e32 v92, v109
	v_exp_f32_e32 v109, v93
	v_add_f32_e32 v83, v107, v83
	v_add_f32_e32 v82, v91, v82
	v_exp_f32_e32 v93, v110
	v_exp_f32_e32 v110, v94
	v_add_f32_e32 v83, v108, v83
	v_add_f32_e32 v82, v92, v82
	v_exp_f32_e32 v94, v111
	v_exp_f32_e32 v111, v95
	v_add_f32_e32 v83, v109, v83
	v_add_f32_e32 v82, v93, v82
	v_exp_f32_e32 v95, v112
	v_exp_f32_e32 v112, v96
	v_add_f32_e32 v83, v110, v83
	v_add_f32_e32 v82, v94, v82
	v_exp_f32_e32 v96, v113
	v_add_f32_e32 v83, v111, v83
	v_add_f32_e32 v82, v95, v82
	v_exp_f32_e32 v113, v97
	v_add_f32_e32 v83, v112, v83
	v_add_f32_e32 v82, v96, v82
	v_cvt_pk_bf16_f32 v84, v98, v99
	v_cvt_pk_bf16_f32 v85, v100, v101
	v_cvt_pk_bf16_f32 v86, v102, v86
	v_cvt_pk_bf16_f32 v87, v87, v88
	v_cvt_pk_bf16_f32 v88, v89, v90
	v_cvt_pk_bf16_f32 v89, v91, v92
	v_cvt_pk_bf16_f32 v90, v93, v94
	v_cvt_pk_bf16_f32 v91, v95, v96
	v_cvt_pk_bf16_f32 v92, v159, v163
	v_cvt_pk_bf16_f32 v93, v161, v165
	v_cvt_pk_bf16_f32 v94, v167, v103
	v_cvt_pk_bf16_f32 v95, v104, v105
	v_cvt_pk_bf16_f32 v96, v106, v107
	v_cvt_pk_bf16_f32 v97, v108, v109
	v_cvt_pk_bf16_f32 v98, v110, v111
	v_cvt_pk_bf16_f32 v99, v112, v113
	v_add_u32_e32 v112, s13, v199
	v_add_f32_e32 v83, v113, v83
	s_waitcnt lgkmcnt(0)
	v_mfma_f32_32x32x16_bf16 v[66:81], v[84:87], v[226:229], v[66:81]
	ds_read_b64_tr_b16 v[100:101], v112 offset:0x200
	ds_read_b64_tr_b16 v[102:103], v112 offset:0xa00
	v_mfma_f32_32x32x16_bf16 v[66:81], v[88:91], v[230:233], v[66:81]
	ds_read_b64_tr_b16 v[104:105], v112 offset:0x1200
	ds_read_b64_tr_b16 v[106:107], v112 offset:0x1a00
	v_mfma_f32_32x32x16_bf16 v[66:81], v[92:95], v[234:237], v[66:81]
	ds_read_b64_tr_b16 v[108:109], v112 offset:0x2200
	ds_read_b64_tr_b16 v[110:111], v112 offset:0x2a00
	ds_read_b64_tr_b16 v[222:223], v112 offset:0x3200
	ds_read_b64_tr_b16 v[224:225], v112 offset:0x3a00
	v_mfma_f32_32x32x16_bf16 v[66:81], v[96:99], v[238:241], v[66:81]
	s_waitcnt lgkmcnt(6)
	v_mfma_f32_32x32x16_bf16 v[50:65], v[84:87], v[100:103], v[50:65]
	ds_read_b64_tr_b16 v[100:101], v112 offset:0x400
	ds_read_b64_tr_b16 v[102:103], v112 offset:0xc00
	s_waitcnt lgkmcnt(6)
	v_mfma_f32_32x32x16_bf16 v[50:65], v[88:91], v[104:107], v[50:65]
	ds_read_b64_tr_b16 v[104:105], v112 offset:0x1400
	ds_read_b64_tr_b16 v[106:107], v112 offset:0x1c00
	s_waitcnt lgkmcnt(6)
	v_mfma_f32_32x32x16_bf16 v[50:65], v[92:95], v[108:111], v[50:65]
	ds_read_b64_tr_b16 v[108:109], v112 offset:0x2400
	ds_read_b64_tr_b16 v[110:111], v112 offset:0x2c00
	ds_read_b64_tr_b16 v[218:219], v112 offset:0x3400
	ds_read_b64_tr_b16 v[220:221], v112 offset:0x3c00
	s_waitcnt lgkmcnt(8)
; #define PSUB_AT(k) do { if (PROBE_SUB == (k) && DK == PROBE_SUBDK) sacc = __builtin_amdgcn_readfirstlane(sacc + ((unsigned)__builtin_readcyclecounter() - ps_t0_)); } while (0)
; #define SWRITE(b) do { _Pragma("unroll") for (int i = 0; i < KP; ++i) *reinterpret_cast<u32x4*>(K_lds + (b) * SHM_K + kst[i]) = ks[i]; \
;         *reinterpret_cast<u32x4*>(V_lds + (b) * SHM_V + vst0) = vs0; *reinterpret_cast<u32x4*>(V_lds + (b) * SHM_V + vst0 + vst1d) = vs1; } while (0)
; template <int DK, bool PF, bool EARLY, bool PFD = false> ...
;     ...
;         pv_one<0>(o[0], vb, pa0, pa1, pa2, pa3); pv_one<1>(o[1], vb, pa0, pa1, pa2, pa3); pv_one<2>(o[2], vb, pa0, pa1, pa2, pa3); pv_one<3>(o[3], vb, pa0, pa1, pa2, pa3);
;         PSUB_AT(3);
;         if (j + 1 < ntile) SWRITE(cur ^ 1);
;         if (j + 3 < ntile) PREFETCH(j + 3);
;         __syncthreads();
	v_mfma_f32_32x32x16_bf16 v[50:65], v[96:99], v[222:225], v[50:65]
	s_waitcnt lgkmcnt(6)
	v_mfma_f32_32x32x16_bf16 v[34:49], v[84:87], v[100:103], v[34:49]
	ds_read_b64_tr_b16 v[100:101], v112 offset:0x600
	ds_read_b64_tr_b16 v[102:103], v112 offset:0xe00
	s_waitcnt lgkmcnt(6)
	v_mfma_f32_32x32x16_bf16 v[34:49], v[88:91], v[104:107], v[34:49]
	ds_read_b64_tr_b16 v[104:105], v112 offset:0x1600
	ds_read_b64_tr_b16 v[106:107], v112 offset:0x1e00
	s_waitcnt lgkmcnt(6)
	v_mfma_f32_32x32x16_bf16 v[34:49], v[92:95], v[108:111], v[34:49]
	ds_read_b64_tr_b16 v[108:109], v112 offset:0x2600
	ds_read_b64_tr_b16 v[110:111], v112 offset:0x2e00
	ds_read_b64_tr_b16 v[222:223], v112 offset:0x3600
	ds_read_b64_tr_b16 v[224:225], v112 offset:0x3e00
	s_waitcnt lgkmcnt(8)
	v_mfma_f32_32x32x16_bf16 v[34:49], v[96:99], v[218:221], v[34:49]
	s_waitcnt lgkmcnt(6)
	v_mfma_f32_32x32x16_bf16 v[18:33], v[84:87], v[100:103], v[18:33]
	s_waitcnt lgkmcnt(0)
	s_xor_b32 s12, s12, 0x2000
	v_add_u32_e32 v84, s12, v196
	s_xor_b32 s12, s13, 0x4000
	s_cmpk_lt_u32 s50, 0x41
	s_waitcnt vmcnt(2)
	ds_write_b128 v84, v[130:133]
	v_add_u32_e32 v84, s12, v197
	s_cselect_b64 s[12:13], -1, 0
	v_mfma_f32_32x32x16_bf16 v[18:33], v[88:91], v[104:107], v[18:33]
	s_and_b64 s[36:37], s[6:7], s[12:13]
	s_waitcnt vmcnt(1)
	ds_write_b128 v84, v[134:137]
	s_waitcnt vmcnt(0)
	ds_write_b128 v84, v[138:141] offset:8192
	v_mfma_f32_32x32x16_bf16 v[18:33], v[92:95], v[108:111], v[18:33]
	v_mfma_f32_32x32x16_bf16 v[18:33], v[96:99], v[222:225], v[18:33]
	s_and_saveexec_b64 s[12:13], s[36:37]
	s_cbranch_execz .LBB0_1931
	s_and_saveexec_b64 s[36:37], s[26:27]
	s_xor_b64 s[36:37], exec, s[36:37]
	s_lshl_b32 s33, s50, 6
	s_addk_i32 s33, 0xc0
	v_add_u32_e32 v84, s33, v189
	v_mul_lo_u32 v84, v84, s42
	v_or_b32_e32 v84, v84, v190
	v_lshl_add_u32 v84, v84, 1, s49
	s_andn2_saveexec_b64 s[36:37], s[36:37]
	s_cbranch_execz .LBB0_1930
	v_add_u32_e32 v84, s51, v206
	s_branch .LBB0_1930
.LBB0_1937:
	v_add_u32_e32 v86, v198, v187
	ds_read_b128 v[82:85], v86 offset:8192
	ds_read_b128 v[130:133], v86 offset:12288
	s_waitcnt lgkmcnt(1)
	v_mfma_f32_32x32x16_bf16 v[98:113], v[82:85], v[126:129], v[2:17]
	s_waitcnt lgkmcnt(0)
	v_mfma_f32_32x32x16_bf16 v[82:97], v[130:133], v[126:129], v[2:17]
	v_add_u32_e32 v130, v198, v200
	ds_read_b128 v[126:129], v130 offset:8192
	s_waitcnt lgkmcnt(0)
	v_mfma_f32_32x32x16_bf16 v[98:113], v[126:129], v[122:125], v[98:113]
	ds_read_b128 v[126:129], v130 offset:12288
	s_waitcnt lgkmcnt(0)
	v_mfma_f32_32x32x16_bf16 v[82:97], v[126:129], v[122:125], v[82:97]
	v_add_u32_e32 v126, v198, v201
	ds_read_b128 v[122:125], v126 offset:8192
	s_waitcnt lgkmcnt(0)
	v_mfma_f32_32x32x16_bf16 v[98:113], v[122:125], v[118:121], v[98:113]
	ds_read_b128 v[122:125], v126 offset:12288
	s_waitcnt lgkmcnt(0)
	v_mfma_f32_32x32x16_bf16 v[82:97], v[122:125], v[118:121], v[82:97]
	v_add_u32_e32 v122, v198, v202
	ds_read_b128 v[118:121], v122 offset:8192
	s_waitcnt lgkmcnt(0)
	v_mfma_f32_32x32x16_bf16 v[98:113], v[118:121], v[114:117], v[98:113]
	ds_read_b128 v[118:121], v122 offset:12288
	s_waitcnt lgkmcnt(0)
; __device__ __forceinline__ float bf2f(bf16 v) { return __uint_as_float((unsigned)v << 16); }
; __device__ __forceinline__ bf16 f2bf(float f) { unsigned u = __float_as_uint(f); return (bf16)((u + 0x7fffu + ((u >> 16) & 1u)) >> 16); }
; #define PSUB_AT(k) do { if (PROBE_SUB == (k) && DK == PROBE_SUBDK) sacc = __builtin_amdgcn_readfirstlane(sacc + ((unsigned)__builtin_readcyclecounter() - ps_t0_)); } while (0)
; template <int DK, bool PF, bool EARLY, bool PFD = false> ...
;     ...
;         float ps = 0.f, ps1 = 0.f;
; #pragma unroll
;         for (int r = 0; r < 16; ++r) { p0[r] = __builtin_amdgcn_exp2f(p0[r]); p1[r] = __builtin_amdgcn_exp2f(p1[r]); ps += p0[r]; asm("" : "+v"(ps)); ps1 += p1[r]; asm("" : "+v"(ps1)); }
;         l_reg += ps + ps1;
;         bf16x8 pa0, pa1, pa2, pa3;
;     ...
;         PK4(p0, 0, pa0); PK4(p0, 8, pa1); PK4(p1, 0, pa2); PK4(p1, 8, pa3);
;     ...
;         PSUB_AT(2);
;         const int vb = vb0 + cur * SHM_V;
;         pv_one<0>(o[0], vb, pa0, pa1, pa2, pa3); pv_one<1>(o[1], vb, pa0, pa1, pa2, pa3); pv_one<2>(o[2], vb, pa0, pa1, pa2, pa3); pv_one<3>(o[3], vb, pa0, pa1, pa2, pa3);
;         PSUB_AT(3);
;         if (j + 1 < ntile) SWRITE(cur ^ 1);
;         if (j + 3 < ntile) PREFETCH(j + 3);
;         __syncthreads();
;         PSUB_AT(4);
;     }
;     __builtin_amdgcn_s_setprio(0);
;     if (PF && !PFD) asm volatile("s_waitcnt vmcnt(0)" : "+v"(pf_dummy) :: "memory");
;     ...
; }
; __device__ __forceinline__ void row_recip(float l_reg, float* li_l  , int r32, int hi, float (&rli)[16]) {
;     { auto rr = __builtin_amdgcn_permlane32_swap(__float_as_uint(l_reg), __float_as_uint(l_reg), false, false); l_reg = __uint_as_float(rr[0]) + __uint_as_float(rr[1]); }
;     if (hi == 0) li_l[r32] = l_reg;
;     asm volatile("s_waitcnt lgkmcnt(0)" ::: "memory");
; #pragma unroll
;     for (int r = 0; r < 16; ++r) rli[r] = __builtin_amdgcn_rcpf(li_l[crow(r, hi)]);
; __device__ __forceinline__ void diff_attn_unit(const Ptrs& P, unsigned char* lds, int b, int h, int qb, unsigned& sacc) {
;     ...
;         float rli[16]; row_recip(l_reg, li_l, r32, hi, rli);
; #pragma unroll
;         for (int r = 0; r < 16; ++r) { const int orow = crow(r, hi);
; #pragma unroll
;             for (int d0 = 0; d0 < 4; ++d0) { bf16* s = stg + orow * 128 + d0 * 32 + r32; const float on = o[d0][r] * rli[r];
;                 if (part == 0) *s = f2bf(on); else *s = f2bf(bf2f(*s) - lam * on); } }
	v_mfma_f32_32x32x16_bf16 v[82:97], v[118:121], v[114:117], v[82:97]
	s_nop 11
	v_exp_f32_e32 v114, v82
	v_exp_f32_e32 v98, v98
	v_exp_f32_e32 v83, v83
	v_exp_f32_e32 v99, v99
	v_add_f32_e32 v115, 0, v114
	v_exp_f32_e32 v116, v84
	v_add_f32_e32 v82, 0, v98
	v_exp_f32_e32 v100, v100
	v_add_f32_e32 v115, v83, v115
	v_exp_f32_e32 v101, v101
	v_add_f32_e32 v82, v99, v82
	v_add_f32_e32 v84, v116, v115
	v_exp_f32_e32 v115, v85
	v_exp_f32_e32 v102, v102
	v_add_f32_e32 v82, v100, v82
	v_exp_f32_e32 v117, v86
	v_exp_f32_e32 v86, v103
	v_add_f32_e32 v82, v101, v82
	v_add_f32_e32 v84, v115, v84
	v_exp_f32_e32 v103, v87
	v_exp_f32_e32 v87, v104
	v_add_f32_e32 v82, v102, v82
	v_add_f32_e32 v84, v117, v84
	v_exp_f32_e32 v104, v88
	v_exp_f32_e32 v88, v105
	v_add_f32_e32 v82, v86, v82
	v_add_f32_e32 v84, v103, v84
	v_exp_f32_e32 v105, v89
	v_exp_f32_e32 v89, v106
	v_add_f32_e32 v82, v87, v82
	v_add_f32_e32 v84, v104, v84
	v_exp_f32_e32 v106, v90
	v_exp_f32_e32 v90, v107
	v_add_f32_e32 v82, v88, v82
	v_add_f32_e32 v84, v105, v84
	v_exp_f32_e32 v107, v91
	v_exp_f32_e32 v91, v108
	v_add_f32_e32 v82, v89, v82
	v_add_f32_e32 v84, v106, v84
	v_exp_f32_e32 v108, v92
	v_exp_f32_e32 v92, v109
	v_add_f32_e32 v82, v90, v82
	v_add_f32_e32 v84, v107, v84
	v_exp_f32_e32 v109, v93
	v_exp_f32_e32 v93, v110
	v_add_f32_e32 v82, v91, v82
	v_add_f32_e32 v84, v108, v84
	v_exp_f32_e32 v110, v94
	v_exp_f32_e32 v94, v111
	v_add_f32_e32 v82, v92, v82
	v_add_f32_e32 v84, v109, v84
	v_exp_f32_e32 v111, v95
	v_exp_f32_e32 v95, v112
	v_add_f32_e32 v82, v93, v82
	v_add_f32_e32 v84, v110, v84
	v_exp_f32_e32 v112, v96
	v_exp_f32_e32 v96, v113
	v_add_f32_e32 v82, v94, v82
	v_add_f32_e32 v84, v111, v84
	v_exp_f32_e32 v113, v97
	s_nop 0
	v_add_f32_e32 v82, v95, v82
	v_add_f32_e32 v84, v112, v84
	s_nop 0
	v_add_f32_e32 v82, v96, v82
	v_add_f32_e32 v84, v113, v84
	s_nop 0
	v_add_f32_e32 v82, v82, v84
	v_cvt_pk_bf16_f32 v84, v98, v99
	v_cvt_pk_bf16_f32 v85, v100, v101
	v_cvt_pk_bf16_f32 v86, v102, v86
	v_cvt_pk_bf16_f32 v87, v87, v88
	v_cvt_pk_bf16_f32 v88, v89, v90
	v_cvt_pk_bf16_f32 v89, v91, v92
	v_cvt_pk_bf16_f32 v90, v93, v94
	v_cvt_pk_bf16_f32 v91, v95, v96
	v_cvt_pk_bf16_f32 v92, v114, v83
	v_cvt_pk_bf16_f32 v93, v116, v115
	v_cvt_pk_bf16_f32 v94, v117, v103
	v_cvt_pk_bf16_f32 v95, v104, v105
	v_cvt_pk_bf16_f32 v96, v106, v107
	v_cvt_pk_bf16_f32 v97, v108, v109
	v_cvt_pk_bf16_f32 v98, v110, v111
	v_cvt_pk_bf16_f32 v99, v112, v113
	ds_read_b64_tr_b16 v[100:101], v203 offset:0
	ds_read_b64_tr_b16 v[102:103], v203 offset:0x800
	ds_read_b64_tr_b16 v[104:105], v203 offset:0x1000
	ds_read_b64_tr_b16 v[106:107], v203 offset:0x1800
	ds_read_b64_tr_b16 v[108:109], v203 offset:0x2000
	ds_read_b64_tr_b16 v[110:111], v203 offset:0x2800
	ds_read_b64_tr_b16 v[112:113], v203 offset:0x3000
	ds_read_b64_tr_b16 v[114:115], v203 offset:0x3800
	s_waitcnt lgkmcnt(0)
	v_add_f32_e32 v82, v142, v82
	v_mfma_f32_32x32x16_bf16 v[66:81], v[84:87], v[100:103], v[66:81]
	ds_read_b64_tr_b16 v[100:101], v203 offset:0x200
	ds_read_b64_tr_b16 v[102:103], v203 offset:0xa00
	v_mfma_f32_32x32x16_bf16 v[66:81], v[88:91], v[104:107], v[66:81]
	ds_read_b64_tr_b16 v[104:105], v203 offset:0x1200
	ds_read_b64_tr_b16 v[106:107], v203 offset:0x1a00
	v_mfma_f32_32x32x16_bf16 v[66:81], v[92:95], v[108:111], v[66:81]
	ds_read_b64_tr_b16 v[108:109], v203 offset:0x2200
	ds_read_b64_tr_b16 v[110:111], v203 offset:0x2a00
	ds_read_b64_tr_b16 v[116:117], v203 offset:0x3200
	ds_read_b64_tr_b16 v[118:119], v203 offset:0x3a00
	s_waitcnt lgkmcnt(0)
	v_mfma_f32_32x32x16_bf16 v[66:81], v[96:99], v[112:115], v[66:81]
	v_mfma_f32_32x32x16_bf16 v[50:65], v[84:87], v[100:103], v[50:65]
	ds_read_b64_tr_b16 v[100:101], v203 offset:0x400
	ds_read_b64_tr_b16 v[102:103], v203 offset:0xc00
	v_mfma_f32_32x32x16_bf16 v[50:65], v[88:91], v[104:107], v[50:65]
	ds_read_b64_tr_b16 v[104:105], v203 offset:0x1400
	ds_read_b64_tr_b16 v[106:107], v203 offset:0x1c00
	v_mfma_f32_32x32x16_bf16 v[50:65], v[92:95], v[108:111], v[50:65]
	ds_read_b64_tr_b16 v[108:109], v203 offset:0x2400
	ds_read_b64_tr_b16 v[110:111], v203 offset:0x2c00
	ds_read_b64_tr_b16 v[112:113], v203 offset:0x3400
	ds_read_b64_tr_b16 v[114:115], v203 offset:0x3c00
	s_waitcnt lgkmcnt(0)
	v_mfma_f32_32x32x16_bf16 v[50:65], v[96:99], v[116:119], v[50:65]
	v_mfma_f32_32x32x16_bf16 v[34:49], v[84:87], v[100:103], v[34:49]
	ds_read_b64_tr_b16 v[100:101], v203 offset:0x600
	ds_read_b64_tr_b16 v[102:103], v203 offset:0xe00
	v_mfma_f32_32x32x16_bf16 v[34:49], v[88:91], v[104:107], v[34:49]
	ds_read_b64_tr_b16 v[104:105], v203 offset:0x1600
	ds_read_b64_tr_b16 v[106:107], v203 offset:0x1e00
	v_mfma_f32_32x32x16_bf16 v[34:49], v[92:95], v[108:111], v[34:49]
	ds_read_b64_tr_b16 v[108:109], v203 offset:0x2600
	ds_read_b64_tr_b16 v[110:111], v203 offset:0x2e00
	ds_read_b64_tr_b16 v[116:117], v203 offset:0x3600
	ds_read_b64_tr_b16 v[118:119], v203 offset:0x3e00
	s_waitcnt lgkmcnt(0)
	v_mfma_f32_32x32x16_bf16 v[34:49], v[96:99], v[112:115], v[34:49]
	v_mfma_f32_32x32x16_bf16 v[18:33], v[84:87], v[100:103], v[18:33]
	s_barrier
	v_mfma_f32_32x32x16_bf16 v[18:33], v[88:91], v[104:107], v[18:33]
	v_mfma_f32_32x32x16_bf16 v[18:33], v[92:95], v[108:111], v[18:33]
	v_mfma_f32_32x32x16_bf16 v[18:33], v[96:99], v[116:119], v[18:33]
	s_setprio 0
	v_mov_b32_e32 v83, v82
	s_nop 1
	v_permlane32_swap_b32_e32 v82, v83
	s_and_saveexec_b64 s[12:13], s[10:11]
	v_add_f32_e32 v82, v82, v83
	ds_write_b32 v204, v82
	s_or_b64 exec, exec, s[12:13]
	s_waitcnt lgkmcnt(0)
	ds_read_b128 v[94:97], v208
	ds_read_b128 v[90:93], v208 offset:32
	ds_read_b128 v[86:89], v208 offset:64
	ds_read_b128 v[82:85], v208 offset:96
	v_cndmask_b32_e64 v98, 0, 1, s[30:31]
	v_cmp_ne_u32_e64 s[12:13], 1, v98
	s_waitcnt lgkmcnt(3)
	v_rcp_f32_e32 v94, v94
	s_andn2_b64 vcc, exec, s[30:31]
	v_mul_f32_e32 v66, v66, v94
	s_cbranch_vccnz .LBB0_1941
	ds_read_u16 v98, v205
	s_waitcnt lgkmcnt(0)
	v_lshlrev_b32_e32 v98, 16, v98
	v_fma_f32 v66, -v143, v66, v98
